# all attention units moved to the scan phase's idle workgroups; top-k gather loads 16 deep; LN2 / y-assembly LDS staging loads issued together; layer-0 out-proj residual epilogue loads 16 deep
# speedup vs baseline: 1.0191x; 1.0191x over previous
; #define LAS __attribute__((address_space(3)))
; DI void attn_unit(const Args& A, LAS unsigned char* lds, int unit, int tid, int wave, int lane) {
;     const bf16* Z = (const bf16*)(A.ws + WS_Z); bf16* ao = (bf16*)(A.ws + WS_ATTO); float* al = (float*)(A.ws + WS_ATTL);
;     const int x = unit & 15; int r0 = unit >> 4; const int hh = r0 & 3; r0 >>= 2; const int b = r0 % NB, br = r0 / NB;
;     const int dil = br == 0 ? 1 : (br == 1 ? 4 : 16), lsub = SEQ / dil, nblk = lsub / 128;
;     const int res = x / nblk, nbk = x % nblk, l0 = nbk * 128, wbase = l0 - 64;
;     LAS bf16* Qs = (LAS bf16*)(lds + AT_QS); LAS bf16* Ks = (LAS bf16*)(lds + AT_KS); LAS bf16* Vt = (LAS bf16*)(lds + AT_VT); LAS float* btab = (LAS float*)(lds + AT_BT);
;     __syncthreads();
; #pragma unroll
;     for (int i = 0; i < 2; ++i) { const int id = tid + 512 * i, row = id >> 3, ch = id & 7; const int tok = b * SEQ + (l0 + row) * dil + res;
;         *(LAS u32x4_t*)(Qs + row * AT_QLD + ch * 8) = *(const u32x4_t*)(Z + (size_t)tok * ZLD + ZA + hh * 64 + ch * 8); }
;     for (int id = tid; id < 272 * 8; id += NTHR) { const int row = id >> 3, ch = id & 7; const int pos = wbase + row; u32x4_t v = (u32x4_t){0u, 0u, 0u, 0u};
;         if (row < 256 && pos >= 0 && pos < lsub) v = *(const u32x4_t*)(Z + (size_t)(b * SEQ + pos * dil + res) * ZLD + ZA + 256 + hh * 64 + ch * 8);
;         *(LAS u32x4_t*)(Ks + row * AT_QLD + ch * 8) = v; }
;     for (int id = tid; id < 272 * 8; id += NTHR) { const int key = id % 272, ch = id / 272; const int pos = wbase + key; u32x4_t v = (u32x4_t){0u, 0u, 0u, 0u};
;         if (key < 256 && pos >= 0 && pos < lsub) v = *(const u32x4_t*)(Z + (size_t)(b * SEQ + pos * dil + res) * ZLD + ZA + 512 + hh * 64 + ch * 8);
;         LAS bf16* d = Vt + (ch * 8) * AT_VLD + key;
;         d[0] = (bf16)(v.x & 0xffffu); d[AT_VLD] = (bf16)(v.x >> 16); d[2 * AT_VLD] = (bf16)(v.y & 0xffffu); d[3 * AT_VLD] = (bf16)(v.y >> 16);
;         d[4 * AT_VLD] = (bf16)(v.z & 0xffffu); d[5 * AT_VLD] = (bf16)(v.z >> 16); d[6 * AT_VLD] = (bf16)(v.w & 0xffffu); d[7 * AT_VLD] = (bf16)(v.w >> 16); }
;     if (tid < 129) btab[tid] = A.in[I_RELB][t5_bucket((tid - 64) * dil) * 4 + hh] * 1.4426950408889634f;
;     __syncthreads();
.LBB0_244:
	s_cmp_lt_i32 s6, 4
	s_cselect_b64 s[0:1], -1, 0
	v_writelane_b32 v235, s0, 60
	s_nop 1
	v_writelane_b32 v235, s1, 61
	s_and_b64 s[0:1], s[0:1], s[2:3]
	s_andn2_b64 vcc, exec, s[0:1]
	v_writelane_b32 v235, s92, 62
	s_cbranch_vccnz .LBB0_496
	s_cmpk_gt_i32 s50, 0xa0
	s_cselect_b32 s0, 0x600, 0
	s_add_i32 s33, s0, s92
	s_cmpk_gt_i32 s33, 0x5ff
	s_mov_b32 s23, 0
	s_cbranch_scc1 .LBB0_336
	s_mov_b32 s6, s33
	s_mov_b32 s7, s50
	s_movk_i32 s8, 0x600
	v_readlane_b32 s9, v235, 52
	v_readlane_b32 s2, v235, 9
	v_readlane_b32 s3, v235, 10
	v_readlane_b32 s4, v235, 19
	v_readlane_b32 s5, v235, 20
	s_mov_b32 s72, 0x3e38aa3b
	s_mov_b32 s73, 0x3e38aa3b
	v_lshrrev_b32_e32 v2, 3, v0
	v_and_b32_e32 v3, 7, v0
	v_lshlrev_b32_e32 v3, 4, v3
	s_movk_i32 s39, 0x90
	v_mad_u32_u24 v1, v2, s39, v3
	v_and_b32_e32 v5, 0xff, v0
	v_lshrrev_b32_e32 v6, 8, v0
	s_movk_i32 s39, 0x1180
	v_mul_u32_u24_e32 v4, s39, v6
	v_lshl_add_u32 v4, v5, 1, v4
	v_add_u32_e32 v4, 0xe100, v4
	v_lshlrev_b32_e32 v6, 4, v6
	v_lshlrev_b32_e32 v8, 2, v5
	v_add_u32_e32 v8, 0x16d00, v8
	v_subrev_u32_e32 v165, 16, v0
	s_movk_i32 s39, 0x81
	v_cmp_gt_u32_e64 s[42:43], s39, v165
	s_movk_i32 s39, 0xa0
	v_cmp_gt_u32_e64 s[48:49], s39, v0
	v_cmp_gt_u32_e64 s[46:47], 64, v0
	v_cmp_gt_u32_e64 s[44:45], 16, v146
	v_subrev_u32_e32 v165, 0x50, v0
	v_cmp_lt_i32_e32 vcc, 0, v165
	v_mov_b32_e32 v7, 0
	s_nop 0
	v_cndmask_b32_e64 v166, 0, 16, vcc
	v_lshlrev_b32_e32 v167, 0, v165
	v_sub_u32_e32 v168, 0, v167
	v_max_i32_e32 v167, v167, v168
	v_cvt_f32_u32_e32 v168, v167
	v_mul_f32_e32 v168, 0x3e000000, v168
	v_max_f32_e32 v168, 1.0, v168
	v_log_f32_e32 v168, v168
	v_cmp_gt_u32_e32 vcc, 8, v167
	v_mul_f32_e32 v168, 0x3f924925, v168
	v_cvt_i32_f32_e32 v168, v168
	v_min_i32_e32 v168, 7, v168
	v_add_u32_e32 v168, 8, v168
	v_cndmask_b32_e32 v168, v168, v167, vcc
	v_add_u32_e32 v168, v168, v166
	v_lshl_or_b32 v7, v168, 0, v7
	v_lshlrev_b32_e32 v167, 2, v165
	v_sub_u32_e32 v168, 0, v167
	v_max_i32_e32 v167, v167, v168
	v_cvt_f32_u32_e32 v168, v167
	v_mul_f32_e32 v168, 0x3e000000, v168
	v_max_f32_e32 v168, 1.0, v168
	v_log_f32_e32 v168, v168
	v_cmp_gt_u32_e32 vcc, 8, v167
	v_mul_f32_e32 v168, 0x3f924925, v168
	v_cvt_i32_f32_e32 v168, v168
	v_min_i32_e32 v168, 7, v168
	v_add_u32_e32 v168, 8, v168
	v_cndmask_b32_e32 v168, v168, v167, vcc
	v_add_u32_e32 v168, v168, v166
	v_lshl_or_b32 v7, v168, 8, v7
	v_lshlrev_b32_e32 v167, 4, v165
	v_sub_u32_e32 v168, 0, v167
	v_max_i32_e32 v167, v167, v168
	v_cvt_f32_u32_e32 v168, v167
	v_mul_f32_e32 v168, 0x3e000000, v168
	v_max_f32_e32 v168, 1.0, v168
	v_log_f32_e32 v168, v168
	v_cmp_gt_u32_e32 vcc, 8, v167
	v_mul_f32_e32 v168, 0x3f924925, v168
	v_cvt_i32_f32_e32 v168, v168
	v_min_i32_e32 v168, 7, v168
	v_add_u32_e32 v168, 8, v168
	v_cndmask_b32_e32 v168, v168, v167, vcc
	v_add_u32_e32 v168, v168, v166
	v_lshl_or_b32 v7, v168, 16, v7
	v_and_b32_e32 v165, 15, v146
	v_lshrrev_b32_e32 v166, 4, v146
	s_lshl_b32 s39, s9, 4
	v_add_u32_e32 v40, s39, v165
	s_movk_i32 s40, 0x90
	v_mul_u32_u24_e32 v34, s40, v40
	v_lshl_add_u32 v34, v166, 4, v34
	v_lshlrev_b32_e32 v167, 2, v166
	v_sub_u32_e32 v35, v167, v165
	v_lshlrev_b32_e32 v35, 2, v35
	v_add_u32_e32 v35, 0x16d40, v35
	v_add_u32_e32 v167, s39, v167
	v_lshlrev_b32_e32 v36, 2, v167
	v_add_u32_e32 v36, 0x16f80, v36
	s_movk_i32 s40, 0x230
	v_mul_u32_u24_e32 v37, s40, v165
	v_lshl_add_u32 v37, v167, 1, v37
	v_add_u32_e32 v37, 0xe100, v37
	v_add_u32_e32 v9, 0x2300, v37
	v_add_u32_e32 v118, 0x4600, v37
	v_add_u32_e32 v144, 0x6900, v37
	v_xor_b32_e32 v38, 16, v146
	v_lshlrev_b32_e32 v38, 2, v38
	v_xor_b32_e32 v39, 32, v146
	v_lshlrev_b32_e32 v39, 2, v39
	v_lshlrev_b32_e32 v41, 3, v166
	v_mov_b32_e32 v232, 0
	v_mov_b32_e32 v233, 0
	s_movk_i32 s40, 0x230
	v_mul_u32_u24_e32 v168, s40, v0
	v_add_u32_e32 v168, 0xe300, v168
	s_and_saveexec_b64 s[40:41], s[46:47]
	ds_write_b64 v168, v[232:233] offset:0
	ds_write_b64 v168, v[232:233] offset:8
	ds_write_b64 v168, v[232:233] offset:16
	ds_write_b64 v168, v[232:233] offset:24
	s_mov_b64 exec, s[40:41]
	s_and_b32 s39, s6, 15
	s_bfe_u32 s40, s6, 0x20004
	s_bfe_u32 s41, s6, 0x30006
	s_lshr_b32 s74, s6, 9
	s_lshl_b32 s75, s74, 1
	s_add_i32 s16, s75, 13
	s_add_i32 s20, s75, 9
	s_add_i32 s26, s75, 4
	s_lshl_b32 s28, s74, 3
	s_lshr_b32 s29, 0x800, s75
	s_add_i32 s17, s29, -1
	s_sub_i32 s76, 4, s75
	s_lshr_b32 s77, s39, s76
	s_lshr_b32 s78, 16, s75
	s_add_i32 s78, s78, -1
	s_and_b32 s78, s39, s78
	s_lshl_b32 s19, s78, 7
	s_add_i32 s18, s19, 0xffffffc0
	s_lshl_b32 s79, s41, 11
	s_add_i32 s79, s79, s77
	s_lshl_b32 s80, s40, 7
	s_lshl_b32 s27, s40, 2
	s_lshl_b32 s81, s79, 13
	s_add_u32 s81, s81, s80
	s_add_u32 s81, s81, 0x2ca00000
	s_add_u32 s10, s2, s81
	s_addc_u32 s11, s3, 0
	s_lshl_b32 s82, s74, 14
	s_add_i32 s82, s82, s79
	s_lshl_b32 s83, s82, 9
	s_add_u32 s83, s83, s80
	s_add_u32 s83, s83, 0x34a00000
	s_add_u32 s12, s2, s83
	s_addc_u32 s13, s3, 0
	s_lshl_b32 s84, s82, 4
	s_add_u32 s84, s84, s27
	s_add_u32 s84, s84, 0x36200000
	s_add_u32 s14, s2, s84
	s_addc_u32 s15, s3, 0
	v_add_u32_e32 v165, s19, v2
	v_lshl_add_u32 v165, v165, s16, v3
	s_lshl_b32 s85, 64, s16
	global_load_dwordx4 v[120:123], v165, s[10:11]
	v_add_u32_e32 v166, s85, v165
	global_load_dwordx4 v[124:127], v166, s[10:11]
	v_add_u32_e32 v167, s18, v2
	v_med3_i32 v168, v167, 0, s17
	v_lshl_add_u32 v168, v168, s16, v3
	global_load_dwordx4 v[128:131], v168, s[10:11] offset:512
	v_add_u32_e32 v168, 64, v167
	v_med3_i32 v168, v168, 0, s17
	v_lshl_add_u32 v168, v168, s16, v3
	global_load_dwordx4 v[132:135], v168, s[10:11] offset:512
	v_add_u32_e32 v168, 0x80, v167
	v_med3_i32 v168, v168, 0, s17
	v_lshl_add_u32 v168, v168, s16, v3
	global_load_dwordx4 v[136:139], v168, s[10:11] offset:512
	v_add_u32_e32 v168, 0xc0, v167
	v_med3_i32 v168, v168, 0, s17
	v_lshl_add_u32 v168, v168, s16, v3
	global_load_dwordx4 v[140:143], v168, s[10:11] offset:512
	v_add_u32_e32 v169, s18, v5
	v_med3_i32 v169, v169, 0, s17
	v_lshl_add_u32 v169, v169, s16, v6
	global_load_dwordx4 v[148:151], v169, s[10:11] offset:1024
	global_load_dwordx4 v[152:155], v169, s[10:11] offset:1056
	global_load_dwordx4 v[156:159], v169, s[10:11] offset:1088
	global_load_dwordx4 v[160:163], v169, s[10:11] offset:1120
	v_bfe_u32 v171, v7, s28, 8
	v_lshl_add_u32 v171, v171, 4, s27
	s_mov_b64 exec, s[42:43]
	global_load_dword v164, v171, s[4:5]
	s_mov_b64 exec, -1

; DI void attn_unit(const Args& A, LAS unsigned char* lds, int unit, int tid, int wave, int lane) {
;     const bf16* Z = (const bf16*)(A.ws + WS_Z); bf16* ao = (bf16*)(A.ws + WS_ATTO); float* al = (float*)(A.ws + WS_ATTL);
;     const int x = unit & 15; int r0 = unit >> 4; const int hh = r0 & 3; r0 >>= 2; const int b = r0 % NB, br = r0 / NB;
;     const int dil = br == 0 ? 1 : (br == 1 ? 4 : 16), lsub = SEQ / dil, nblk = lsub / 128;
;     const int res = x / nblk, nbk = x % nblk, l0 = nbk * 128, wbase = l0 - 64;
;     LAS bf16* Qs = (LAS bf16*)(lds + AT_QS); LAS bf16* Ks = (LAS bf16*)(lds + AT_KS); LAS bf16* Vt = (LAS bf16*)(lds + AT_VT); LAS float* btab = (LAS float*)(lds + AT_BT);
;     __syncthreads();
; #pragma unroll
;     for (int i = 0; i < 2; ++i) { const int id = tid + 512 * i, row = id >> 3, ch = id & 7; const int tok = b * SEQ + (l0 + row) * dil + res;
;         *(LAS u32x4_t*)(Qs + row * AT_QLD + ch * 8) = *(const u32x4_t*)(Z + (size_t)tok * ZLD + ZA + hh * 64 + ch * 8); }
;     for (int id = tid; id < 272 * 8; id += NTHR) { const int row = id >> 3, ch = id & 7; const int pos = wbase + row; u32x4_t v = (u32x4_t){0u, 0u, 0u, 0u};
;         if (row < 256 && pos >= 0 && pos < lsub) v = *(const u32x4_t*)(Z + (size_t)(b * SEQ + pos * dil + res) * ZLD + ZA + 256 + hh * 64 + ch * 8);
;         *(LAS u32x4_t*)(Ks + row * AT_QLD + ch * 8) = v; }
;     for (int id = tid; id < 272 * 8; id += NTHR) { const int key = id % 272, ch = id / 272; const int pos = wbase + key; u32x4_t v = (u32x4_t){0u, 0u, 0u, 0u};
;         if (key < 256 && pos >= 0 && pos < lsub) v = *(const u32x4_t*)(Z + (size_t)(b * SEQ + pos * dil + res) * ZLD + ZA + 512 + hh * 64 + ch * 8);
;         LAS bf16* d = Vt + (ch * 8) * AT_VLD + key;
;         d[0] = (bf16)(v.x & 0xffffu); d[AT_VLD] = (bf16)(v.x >> 16); d[2 * AT_VLD] = (bf16)(v.y & 0xffffu); d[3 * AT_VLD] = (bf16)(v.y >> 16);
;         d[4 * AT_VLD] = (bf16)(v.z & 0xffffu); d[5 * AT_VLD] = (bf16)(v.z >> 16); d[6 * AT_VLD] = (bf16)(v.w & 0xffffu); d[7 * AT_VLD] = (bf16)(v.w >> 16); }
;     if (tid < 129) btab[tid] = A.in[I_RELB][t5_bucket((tid - 64) * dil) * 4 + hh] * 1.4426950408889634f;
;     __syncthreads();
; template <int l> DI void run_layer(const Args& A, LAS unsigned char* lds, const XcdBarrier& bar, int lo, int hi, int G, int bid, int tid, int lane, int wave, int gw, int ngw, int gtid, int nthr) {
;     ...
;     PH(3,
.LBB0_546:
	s_cmp_lt_i32 s6, 5
	s_cselect_b64 s[94:95], -1, 0
	s_and_b64 s[0:1], s[94:95], s[0:1]
	s_andn2_b64 vcc, exec, s[0:1]
	s_cbranch_vccnz .LBB0_957
	s_cmpk_lt_i32 s50, 0xa1
	s_cselect_b64 s[0:1], -1, 0
	s_cmpk_lt_i32 s92, 0xa0
	s_cselect_b64 s[2:3], -1, 0
	s_or_b64 s[0:1], s[2:3], s[0:1]
	s_and_b64 vcc, exec, s[0:1]
	s_cbranch_vccnz .LBB0_640
	s_add_i32 s22, s92, 0xffffff60
	s_cmpk_gt_u32 s22, 0x23f
	s_cbranch_scc1 .LBB0_639
	s_mov_b32 s6, s22
	s_add_i32 s7, s50, 0xffffff60
	s_movk_i32 s8, 0x600
	v_readlane_b32 s9, v235, 52
	v_readlane_b32 s2, v235, 9
	v_readlane_b32 s3, v235, 10
	v_readlane_b32 s4, v235, 19
	v_readlane_b32 s5, v235, 20
	s_mov_b32 s72, 0x3e38aa3b
	s_mov_b32 s73, 0x3e38aa3b
	v_lshrrev_b32_e32 v2, 3, v0
	v_and_b32_e32 v3, 7, v0
	v_lshlrev_b32_e32 v3, 4, v3
	s_movk_i32 s39, 0x90
	v_mad_u32_u24 v1, v2, s39, v3
	v_and_b32_e32 v5, 0xff, v0
	v_lshrrev_b32_e32 v6, 8, v0
	s_movk_i32 s39, 0x1180
	v_mul_u32_u24_e32 v4, s39, v6
	v_lshl_add_u32 v4, v5, 1, v4
	v_add_u32_e32 v4, 0xe100, v4
	v_lshlrev_b32_e32 v6, 4, v6
	v_lshlrev_b32_e32 v8, 2, v5
	v_add_u32_e32 v8, 0x16d00, v8
	v_subrev_u32_e32 v165, 16, v0
	s_movk_i32 s39, 0x81
	v_cmp_gt_u32_e64 s[42:43], s39, v165
	s_movk_i32 s39, 0xa0
	v_cmp_gt_u32_e64 s[48:49], s39, v0
	v_cmp_gt_u32_e64 s[46:47], 64, v0
	v_cmp_gt_u32_e64 s[44:45], 16, v146
	v_subrev_u32_e32 v165, 0x50, v0
	v_cmp_lt_i32_e32 vcc, 0, v165
	v_mov_b32_e32 v7, 0
	s_nop 0
	v_cndmask_b32_e64 v166, 0, 16, vcc
	v_lshlrev_b32_e32 v167, 0, v165
	v_sub_u32_e32 v168, 0, v167
	v_max_i32_e32 v167, v167, v168
	v_cvt_f32_u32_e32 v168, v167
	v_mul_f32_e32 v168, 0x3e000000, v168
	v_max_f32_e32 v168, 1.0, v168
	v_log_f32_e32 v168, v168
	v_cmp_gt_u32_e32 vcc, 8, v167
	v_mul_f32_e32 v168, 0x3f924925, v168
	v_cvt_i32_f32_e32 v168, v168
	v_min_i32_e32 v168, 7, v168
	v_add_u32_e32 v168, 8, v168
	v_cndmask_b32_e32 v168, v168, v167, vcc
	v_add_u32_e32 v168, v168, v166
	v_lshl_or_b32 v7, v168, 0, v7
	v_lshlrev_b32_e32 v167, 2, v165
	v_sub_u32_e32 v168, 0, v167
	v_max_i32_e32 v167, v167, v168
	v_cvt_f32_u32_e32 v168, v167
	v_mul_f32_e32 v168, 0x3e000000, v168
	v_max_f32_e32 v168, 1.0, v168
	v_log_f32_e32 v168, v168
	v_cmp_gt_u32_e32 vcc, 8, v167
	v_mul_f32_e32 v168, 0x3f924925, v168
	v_cvt_i32_f32_e32 v168, v168
	v_min_i32_e32 v168, 7, v168
	v_add_u32_e32 v168, 8, v168
	v_cndmask_b32_e32 v168, v168, v167, vcc
	v_add_u32_e32 v168, v168, v166
	v_lshl_or_b32 v7, v168, 8, v7
	v_lshlrev_b32_e32 v167, 4, v165
	v_sub_u32_e32 v168, 0, v167
	v_max_i32_e32 v167, v167, v168
	v_cvt_f32_u32_e32 v168, v167
	v_mul_f32_e32 v168, 0x3e000000, v168
	v_max_f32_e32 v168, 1.0, v168
	v_log_f32_e32 v168, v168
	v_cmp_gt_u32_e32 vcc, 8, v167
	v_mul_f32_e32 v168, 0x3f924925, v168
	v_cvt_i32_f32_e32 v168, v168
	v_min_i32_e32 v168, 7, v168
	v_add_u32_e32 v168, 8, v168
	v_cndmask_b32_e32 v168, v168, v167, vcc
	v_add_u32_e32 v168, v168, v166
	v_lshl_or_b32 v7, v168, 16, v7
	v_and_b32_e32 v165, 15, v146
	v_lshrrev_b32_e32 v166, 4, v146
	s_lshl_b32 s39, s9, 4
	v_add_u32_e32 v40, s39, v165
	s_movk_i32 s40, 0x90
	v_mul_u32_u24_e32 v34, s40, v40
	v_lshl_add_u32 v34, v166, 4, v34
	v_lshlrev_b32_e32 v167, 2, v166
	v_sub_u32_e32 v35, v167, v165
	v_lshlrev_b32_e32 v35, 2, v35
	v_add_u32_e32 v35, 0x16d40, v35
	v_add_u32_e32 v167, s39, v167
	v_lshlrev_b32_e32 v36, 2, v167
	v_add_u32_e32 v36, 0x16f80, v36
	s_movk_i32 s40, 0x230
	v_mul_u32_u24_e32 v37, s40, v165
	v_lshl_add_u32 v37, v167, 1, v37
	v_add_u32_e32 v37, 0xe100, v37
	v_add_u32_e32 v9, 0x2300, v37
	v_add_u32_e32 v118, 0x4600, v37
	v_add_u32_e32 v144, 0x6900, v37
	v_xor_b32_e32 v38, 16, v146
	v_lshlrev_b32_e32 v38, 2, v38
	v_xor_b32_e32 v39, 32, v146
	v_lshlrev_b32_e32 v39, 2, v39
	v_lshlrev_b32_e32 v41, 3, v166
	v_mov_b32_e32 v232, 0
	v_mov_b32_e32 v233, 0
	s_movk_i32 s40, 0x230
	v_mul_u32_u24_e32 v168, s40, v0
	v_add_u32_e32 v168, 0xe300, v168
	s_and_saveexec_b64 s[40:41], s[46:47]
	ds_write_b64 v168, v[232:233] offset:0
	ds_write_b64 v168, v[232:233] offset:8
	ds_write_b64 v168, v[232:233] offset:16
	ds_write_b64 v168, v[232:233] offset:24
	s_mov_b64 exec, s[40:41]
	s_and_b32 s39, s6, 15
	s_bfe_u32 s40, s6, 0x20004
	s_bfe_u32 s41, s6, 0x30006
	s_lshr_b32 s74, s6, 9
	s_lshl_b32 s75, s74, 1
	s_add_i32 s16, s75, 13
	s_add_i32 s20, s75, 9
	s_add_i32 s26, s75, 4
	s_lshl_b32 s28, s74, 3
	s_lshr_b32 s29, 0x800, s75
	s_add_i32 s17, s29, -1
	s_sub_i32 s76, 4, s75
	s_lshr_b32 s77, s39, s76
	s_lshr_b32 s78, 16, s75
	s_add_i32 s78, s78, -1
	s_and_b32 s78, s39, s78
	s_lshl_b32 s19, s78, 7
	s_add_i32 s18, s19, 0xffffffc0
	s_lshl_b32 s79, s41, 11
	s_add_i32 s79, s79, s77
	s_lshl_b32 s80, s40, 7
	s_lshl_b32 s27, s40, 2
	s_lshl_b32 s81, s79, 13
	s_add_u32 s81, s81, s80
	s_add_u32 s81, s81, 0x2ca00000
	s_add_u32 s10, s2, s81
	s_addc_u32 s11, s3, 0
	s_lshl_b32 s82, s74, 14
	s_add_i32 s82, s82, s79
	s_lshl_b32 s83, s82, 9
	s_add_u32 s83, s83, s80
	s_add_u32 s83, s83, 0x34a00000
	s_add_u32 s12, s2, s83
	s_addc_u32 s13, s3, 0
	s_lshl_b32 s84, s82, 4
	s_add_u32 s84, s84, s27
	s_add_u32 s84, s84, 0x36200000
	s_add_u32 s14, s2, s84
	s_addc_u32 s15, s3, 0
	v_add_u32_e32 v165, s19, v2
	v_lshl_add_u32 v165, v165, s16, v3
	s_lshl_b32 s85, 64, s16
	global_load_dwordx4 v[120:123], v165, s[10:11]
	v_add_u32_e32 v166, s85, v165
	global_load_dwordx4 v[124:127], v166, s[10:11]
	v_add_u32_e32 v167, s18, v2
	v_med3_i32 v168, v167, 0, s17
	v_lshl_add_u32 v168, v168, s16, v3
	global_load_dwordx4 v[128:131], v168, s[10:11] offset:512
	v_add_u32_e32 v168, 64, v167
	v_med3_i32 v168, v168, 0, s17
	v_lshl_add_u32 v168, v168, s16, v3
	global_load_dwordx4 v[132:135], v168, s[10:11] offset:512
	v_add_u32_e32 v168, 0x80, v167
	v_med3_i32 v168, v168, 0, s17
	v_lshl_add_u32 v168, v168, s16, v3
	global_load_dwordx4 v[136:139], v168, s[10:11] offset:512
	v_add_u32_e32 v168, 0xc0, v167
	v_med3_i32 v168, v168, 0, s17
	v_lshl_add_u32 v168, v168, s16, v3
	global_load_dwordx4 v[140:143], v168, s[10:11] offset:512
	v_add_u32_e32 v169, s18, v5
	v_med3_i32 v169, v169, 0, s17
	v_lshl_add_u32 v169, v169, s16, v6
	global_load_dwordx4 v[148:151], v169, s[10:11] offset:1024
	global_load_dwordx4 v[152:155], v169, s[10:11] offset:1056
	global_load_dwordx4 v[156:159], v169, s[10:11] offset:1088
	global_load_dwordx4 v[160:163], v169, s[10:11] offset:1120
	v_bfe_u32 v171, v7, s28, 8
	v_lshl_add_u32 v171, v171, 4, s27
	s_mov_b64 exec, s[42:43]
	global_load_dword v164, v171, s[4:5]
	s_mov_b64 exec, -1

; #define LAS __attribute__((address_space(3)))
; DI void phase_yasm(const Args& A, int l, LAS unsigned char* lds, int gw, int ngw, int tid, int lane) {
;     ...
;     LAS bf16* G2T = (LAS bf16*)lds;
;     __syncthreads();
;     { const u32x4_t* src = (const u32x4_t*)(A.ws + WS_G2T + (size_t)l * RW * 128 * 2);
;       for (int idx = tid; idx < RW * 16; idx += NTHR) { const int col = idx >> 4, ch = idx & 15; *(LAS u32x4_t*)(G2T + col * YA_G2LD + ch * 8) = src[idx]; } }
;     __syncthreads();
.LBB0_1007:
	s_cmp_lt_i32 s6, 6
	s_cselect_b64 s[16:17], -1, 0
	s_and_b64 s[0:1], s[16:17], s[0:1]
	s_andn2_b64 vcc, exec, s[0:1]
	v_lshrrev_b32_e32 v170, 4, v0
	s_cbranch_vccnz .LBB0_1039
	s_waitcnt vmcnt(0)
	v_lshlrev_b32_e32 v2, 4, v0
	v_mov_b32_e32 v3, 0
	v_and_b32_e32 v1, 15, v0
	v_lshl_add_u64 v[2:3], s[4:5], 0, v[2:3]
	s_mov_b64 s[0:1], 0x2c900000
	v_mul_u32_u24_e32 v5, 0x110, v170
	v_lshlrev_b32_e32 v6, 4, v1
	v_or_b32_e32 v4, 0xfffffe00, v0
	v_lshl_add_u64 v[2:3], v[2:3], 0, s[0:1]
	v_add3_u32 v5, v5, v6, 0
	s_mov_b64 s[0:1], 0
	s_mov_b64 s[2:3], 0x2000
	s_movk_i32 s4, 0x15ff
	s_barrier
	global_load_dwordx4 v[172:175], v[2:3], off
	v_lshl_add_u64 v[2:3], v[2:3], 0, s[2:3]
	global_load_dwordx4 v[176:179], v[2:3], off
	v_lshl_add_u64 v[2:3], v[2:3], 0, s[2:3]
	global_load_dwordx4 v[180:183], v[2:3], off
	v_lshl_add_u64 v[2:3], v[2:3], 0, s[2:3]
	global_load_dwordx4 v[184:187], v[2:3], off
	v_lshl_add_u64 v[2:3], v[2:3], 0, s[2:3]
	global_load_dwordx4 v[188:191], v[2:3], off
	v_lshl_add_u64 v[2:3], v[2:3], 0, s[2:3]
	global_load_dwordx4 v[192:195], v[2:3], off
	v_lshl_add_u64 v[2:3], v[2:3], 0, s[2:3]
	global_load_dwordx4 v[196:199], v[2:3], off
	v_lshl_add_u64 v[2:3], v[2:3], 0, s[2:3]
	global_load_dwordx4 v[200:203], v[2:3], off
	v_lshl_add_u64 v[2:3], v[2:3], 0, s[2:3]
	global_load_dwordx4 v[204:207], v[2:3], off
	v_lshl_add_u64 v[2:3], v[2:3], 0, s[2:3]
	global_load_dwordx4 v[208:211], v[2:3], off
	v_lshl_add_u64 v[2:3], v[2:3], 0, s[2:3]
	global_load_dwordx4 v[212:215], v[2:3], off
	v_lshl_add_u64 v[2:3], v[2:3], 0, s[2:3]
	global_load_dwordx4 v[216:219], v[2:3], off
	v_add_u32_e32 v4, 0x11000, v5
	s_waitcnt vmcnt(0)
	ds_write_b128 v5, v[172:175] offset:0
	ds_write_b128 v5, v[176:179] offset:8704
	ds_write_b128 v5, v[180:183] offset:17408
	ds_write_b128 v5, v[184:187] offset:26112
	ds_write_b128 v5, v[188:191] offset:34816
	ds_write_b128 v5, v[192:195] offset:43520
	ds_write_b128 v5, v[196:199] offset:52224
	ds_write_b128 v5, v[200:203] offset:60928
	ds_write_b128 v4, v[204:207] offset:0
	ds_write_b128 v4, v[208:211] offset:8704
	ds_write_b128 v4, v[212:215] offset:17408
	ds_write_b128 v4, v[216:219] offset:26112
	v_readlane_b32 s4, v235, 9
	v_readlane_b32 s5, v235, 10
	s_add_u32 s18, s4, 0x2ca00000
	s_addc_u32 s19, s5, 0
	s_add_u32 s0, s4, 0x2a600000
	s_addc_u32 s1, s5, 0
	v_readlane_b32 s2, v235, 54
	v_readlane_b32 s6, v235, 11
	v_readlane_b32 s7, v235, 12
	s_cmpk_gt_i32 s2, 0x17ff
	s_waitcnt lgkmcnt(0)
	s_barrier
	v_readlane_b32 s3, v235, 55
	s_cbranch_scc0 .LBB0_1012
	v_lshlrev_b32_e32 v114, 2, v146
	v_lshrrev_b32_e32 v117, 4, v146
	s_cbranch_execz .LBB0_1013
	s_branch .LBB0_1020

; DI unsigned pkbf(float lo, float hi) { typedef __bf16 b2 __attribute__((ext_vector_type(2))); typedef float f2 __attribute__((ext_vector_type(2))); const f2 v = {lo, hi}; return __builtin_bit_cast(unsigned, __builtin_convertvector(v, b2)); }
;     DI void operator()(const pg8::f32x4 (&acc)[2][2][4][2], const pg8::Unit& u, int wr, int wc, int fr, int fq) const {
;         const int row0 = u.pm * 256 + wr * 64 + fr, col0 = u.pn * 256 + wc * 32 + 4 * fq;
; #pragma unroll
;         for (int ai = 0; ai < 2; ++ai)
; #pragma unroll
;             for (int m = 0; m < 4; ++m) { const size_t off = (size_t)(row0 + ai * 128 + m * 16) * ldc + col0;
; #pragma unroll
;                 for (int bj = 0; bj < 2; ++bj)
; #pragma unroll
;                     for (int n = 0; n < 2; ++n) { pg8::f32x4 b;
;                         if constexpr (BASE_BF16) { const uint2 w = *(const uint2*)((const bf16*)base + off + bj * 128 + n * 16);
;                             b[0] = __uint_as_float(w.x << 16); b[1] = __uint_as_float(w.x & 0xffff0000u); b[2] = __uint_as_float(w.y << 16); b[3] = __uint_as_float(w.y & 0xffff0000u); }
;                         else b = *(const pg8::f32x4*)((const float*)base + off + bj * 128 + n * 16);
;                         b += acc[ai][bj][m][n]; uint2 o; o.x = pkbf(b[0], b[1]); o.y = pkbf(b[2], b[3]); *(uint2*)(out + off + bj * 128 + n * 16) = o; } }
;     }
.LBB0_1110:
	v_lshl_add_u32 v148, s20, 8, v1
	v_lshl_or_b32 v144, s21, 8, v151
	v_ashrrev_i32_e32 v149, 31, v148
	v_ashrrev_i32_e32 v145, 31, v144
	v_lshlrev_b64 v[142:143], 10, v[148:149]
	v_readlane_b32 s72, v235, 17
	v_lshl_add_u64 v[142:143], v[142:143], 0, v[144:145]
	v_readlane_b32 s73, v235, 18
	s_mov_b64 s[20:21], 0x20000
	s_andn2_b64 vcc, exec, s[2:3]
	v_lshl_add_u64 v[160:161], v[142:143], 2, s[72:73]
	v_lshl_add_u64 v[240:241], v[142:143], 1, s[6:7]
	s_mov_b64 s[22:23], 0x10000
	s_mov_b64 s[24:25], 0x50000
	s_mov_b64 s[26:27], 0x8000
	s_mov_b64 s[46:47], 0x28000
	global_load_dwordx4 v[172:175], v[160:161], off
	global_load_dwordx4 v[176:179], v[160:161], off offset:64
	global_load_dwordx4 v[180:183], v[160:161], off offset:512
	global_load_dwordx4 v[184:187], v[160:161], off offset:576
	v_lshl_add_u64 v[160:161], v[160:161], 0, s[22:23]
	global_load_dwordx4 v[188:191], v[160:161], off
	global_load_dwordx4 v[192:195], v[160:161], off offset:64
	global_load_dwordx4 v[196:199], v[160:161], off offset:512
	global_load_dwordx4 v[200:203], v[160:161], off offset:576
	v_lshl_add_u64 v[160:161], v[160:161], 0, s[22:23]
	global_load_dwordx4 v[204:207], v[160:161], off
	global_load_dwordx4 v[208:211], v[160:161], off offset:64
	global_load_dwordx4 v[212:215], v[160:161], off offset:512
	global_load_dwordx4 v[216:219], v[160:161], off offset:576
	v_lshl_add_u64 v[160:161], v[160:161], 0, s[22:23]
	global_load_dwordx4 v[220:223], v[160:161], off
	global_load_dwordx4 v[224:227], v[160:161], off offset:64
	global_load_dwordx4 v[228:231], v[160:161], off offset:512
	global_load_dwordx4 v[236:239], v[160:161], off offset:576
	s_waitcnt vmcnt(15)
	v_pk_add_f32 v[126:127], v[126:127], v[172:173]
	v_pk_add_f32 v[128:129], v[128:129], v[174:175]
	v_cvt_pk_bf16_f32 v126, v126, v127
	v_cvt_pk_bf16_f32 v127, v128, v129
	global_store_dwordx2 v[240:241], v[126:127], off
	s_waitcnt vmcnt(15)
	v_pk_add_f32 v[122:123], v[122:123], v[176:177]
	v_pk_add_f32 v[124:125], v[124:125], v[178:179]
	v_cvt_pk_bf16_f32 v122, v122, v123
	v_cvt_pk_bf16_f32 v123, v124, v125
	global_store_dwordx2 v[240:241], v[122:123], off offset:32
	s_waitcnt vmcnt(15)
	v_pk_add_f32 v[118:119], v[118:119], v[180:181]
	v_pk_add_f32 v[120:121], v[120:121], v[182:183]
	v_cvt_pk_bf16_f32 v118, v118, v119
	v_cvt_pk_bf16_f32 v119, v120, v121
	global_store_dwordx2 v[240:241], v[118:119], off offset:256
	s_waitcnt vmcnt(15)
	v_pk_add_f32 v[114:115], v[114:115], v[184:185]
	v_pk_add_f32 v[116:117], v[116:117], v[186:187]
	v_cvt_pk_bf16_f32 v114, v114, v115
	v_cvt_pk_bf16_f32 v115, v116, v117
	global_store_dwordx2 v[240:241], v[114:115], off offset:288
	v_lshl_add_u64 v[160:161], v[160:161], 0, s[24:25]
	global_load_dwordx4 v[172:175], v[160:161], off
	global_load_dwordx4 v[176:179], v[160:161], off offset:64
	global_load_dwordx4 v[180:183], v[160:161], off offset:512
	global_load_dwordx4 v[184:187], v[160:161], off offset:576
	v_lshl_add_u64 v[240:241], v[240:241], 0, s[26:27]
	s_waitcnt vmcnt(19)
	v_pk_add_f32 v[110:111], v[110:111], v[188:189]
	v_pk_add_f32 v[112:113], v[112:113], v[190:191]
	v_cvt_pk_bf16_f32 v110, v110, v111
	v_cvt_pk_bf16_f32 v111, v112, v113
	global_store_dwordx2 v[240:241], v[110:111], off
	s_waitcnt vmcnt(19)
	v_pk_add_f32 v[106:107], v[106:107], v[192:193]
	v_pk_add_f32 v[108:109], v[108:109], v[194:195]
	v_cvt_pk_bf16_f32 v106, v106, v107
	v_cvt_pk_bf16_f32 v107, v108, v109
	global_store_dwordx2 v[240:241], v[106:107], off offset:32
	s_waitcnt vmcnt(19)
	v_pk_add_f32 v[102:103], v[102:103], v[196:197]
	v_pk_add_f32 v[104:105], v[104:105], v[198:199]
	v_cvt_pk_bf16_f32 v102, v102, v103
	v_cvt_pk_bf16_f32 v103, v104, v105
	global_store_dwordx2 v[240:241], v[102:103], off offset:256
	s_waitcnt vmcnt(19)
	v_pk_add_f32 v[98:99], v[98:99], v[200:201]
	v_pk_add_f32 v[100:101], v[100:101], v[202:203]
	v_cvt_pk_bf16_f32 v98, v98, v99
	v_cvt_pk_bf16_f32 v99, v100, v101
	global_store_dwordx2 v[240:241], v[98:99], off offset:288
	v_lshl_add_u64 v[160:161], v[160:161], 0, s[22:23]
	global_load_dwordx4 v[188:191], v[160:161], off
	global_load_dwordx4 v[192:195], v[160:161], off offset:64
	global_load_dwordx4 v[196:199], v[160:161], off offset:512
	global_load_dwordx4 v[200:203], v[160:161], off offset:576
	v_lshl_add_u64 v[240:241], v[240:241], 0, s[26:27]
	s_waitcnt vmcnt(23)
	v_pk_add_f32 v[94:95], v[94:95], v[204:205]
	v_pk_add_f32 v[96:97], v[96:97], v[206:207]
	v_cvt_pk_bf16_f32 v94, v94, v95
	v_cvt_pk_bf16_f32 v95, v96, v97
	global_store_dwordx2 v[240:241], v[94:95], off
	s_waitcnt vmcnt(23)
	v_pk_add_f32 v[90:91], v[90:91], v[208:209]
	v_pk_add_f32 v[92:93], v[92:93], v[210:211]
	v_cvt_pk_bf16_f32 v90, v90, v91
	v_cvt_pk_bf16_f32 v91, v92, v93
	global_store_dwordx2 v[240:241], v[90:91], off offset:32
	s_waitcnt vmcnt(23)
	v_pk_add_f32 v[86:87], v[86:87], v[212:213]
	v_pk_add_f32 v[88:89], v[88:89], v[214:215]
	v_cvt_pk_bf16_f32 v86, v86, v87
	v_cvt_pk_bf16_f32 v87, v88, v89
	global_store_dwordx2 v[240:241], v[86:87], off offset:256
	s_waitcnt vmcnt(23)
	v_pk_add_f32 v[82:83], v[82:83], v[216:217]
	v_pk_add_f32 v[84:85], v[84:85], v[218:219]
	v_cvt_pk_bf16_f32 v82, v82, v83
	v_cvt_pk_bf16_f32 v83, v84, v85
	global_store_dwordx2 v[240:241], v[82:83], off offset:288
	v_lshl_add_u64 v[160:161], v[160:161], 0, s[22:23]
	global_load_dwordx4 v[204:207], v[160:161], off
	global_load_dwordx4 v[208:211], v[160:161], off offset:64
	global_load_dwordx4 v[212:215], v[160:161], off offset:512
	global_load_dwordx4 v[216:219], v[160:161], off offset:576
	v_lshl_add_u64 v[240:241], v[240:241], 0, s[26:27]
	s_waitcnt vmcnt(27)
; DI unsigned pkbf(float lo, float hi) { typedef __bf16 b2 __attribute__((ext_vector_type(2))); typedef float f2 __attribute__((ext_vector_type(2))); const f2 v = {lo, hi}; return __builtin_bit_cast(unsigned, __builtin_convertvector(v, b2)); }
;     DI void operator()(const pg8::f32x4 (&acc)[2][2][4][2], const pg8::Unit& u, int wr, int wc, int fr, int fq) const {
;         const int row0 = u.pm * 256 + wr * 64 + fr, col0 = u.pn * 256 + wc * 32 + 4 * fq;
; #pragma unroll
;         for (int ai = 0; ai < 2; ++ai)
; #pragma unroll
;             for (int m = 0; m < 4; ++m) { const size_t off = (size_t)(row0 + ai * 128 + m * 16) * ldc + col0;
; #pragma unroll
;                 for (int bj = 0; bj < 2; ++bj)
; #pragma unroll
;                     for (int n = 0; n < 2; ++n) { pg8::f32x4 b;
;                         if constexpr (BASE_BF16) { const uint2 w = *(const uint2*)((const bf16*)base + off + bj * 128 + n * 16);
;                             b[0] = __uint_as_float(w.x << 16); b[1] = __uint_as_float(w.x & 0xffff0000u); b[2] = __uint_as_float(w.y << 16); b[3] = __uint_as_float(w.y & 0xffff0000u); }
;                         else b = *(const pg8::f32x4*)((const float*)base + off + bj * 128 + n * 16);
;                         b += acc[ai][bj][m][n]; uint2 o; o.x = pkbf(b[0], b[1]); o.y = pkbf(b[2], b[3]); *(uint2*)(out + off + bj * 128 + n * 16) = o; } }
;     }
	v_pk_add_f32 v[78:79], v[78:79], v[220:221]
	v_pk_add_f32 v[80:81], v[80:81], v[222:223]
	v_cvt_pk_bf16_f32 v78, v78, v79
	v_cvt_pk_bf16_f32 v79, v80, v81
	global_store_dwordx2 v[240:241], v[78:79], off
	s_waitcnt vmcnt(27)
	v_pk_add_f32 v[74:75], v[74:75], v[224:225]
	v_pk_add_f32 v[76:77], v[76:77], v[226:227]
	v_cvt_pk_bf16_f32 v74, v74, v75
	v_cvt_pk_bf16_f32 v75, v76, v77
	global_store_dwordx2 v[240:241], v[74:75], off offset:32
	s_waitcnt vmcnt(27)
	v_pk_add_f32 v[70:71], v[70:71], v[228:229]
	v_pk_add_f32 v[72:73], v[72:73], v[230:231]
	v_cvt_pk_bf16_f32 v70, v70, v71
	v_cvt_pk_bf16_f32 v71, v72, v73
	global_store_dwordx2 v[240:241], v[70:71], off offset:256
	s_waitcnt vmcnt(27)
	v_pk_add_f32 v[66:67], v[66:67], v[236:237]
	v_pk_add_f32 v[68:69], v[68:69], v[238:239]
	v_cvt_pk_bf16_f32 v66, v66, v67
	v_cvt_pk_bf16_f32 v67, v68, v69
	global_store_dwordx2 v[240:241], v[66:67], off offset:288
	v_lshl_add_u64 v[160:161], v[160:161], 0, s[22:23]
	global_load_dwordx4 v[220:223], v[160:161], off
	global_load_dwordx4 v[224:227], v[160:161], off offset:64
	global_load_dwordx4 v[228:231], v[160:161], off offset:512
	global_load_dwordx4 v[236:239], v[160:161], off offset:576
	v_lshl_add_u64 v[240:241], v[240:241], 0, s[46:47]
	s_waitcnt vmcnt(27)
	v_pk_add_f32 v[62:63], v[62:63], v[172:173]
	v_pk_add_f32 v[64:65], v[64:65], v[174:175]
	v_cvt_pk_bf16_f32 v62, v62, v63
	v_cvt_pk_bf16_f32 v63, v64, v65
	global_store_dwordx2 v[240:241], v[62:63], off
	s_waitcnt vmcnt(27)
	v_pk_add_f32 v[58:59], v[58:59], v[176:177]
	v_pk_add_f32 v[60:61], v[60:61], v[178:179]
	v_cvt_pk_bf16_f32 v58, v58, v59
	v_cvt_pk_bf16_f32 v59, v60, v61
	global_store_dwordx2 v[240:241], v[58:59], off offset:32
	s_waitcnt vmcnt(27)
	v_pk_add_f32 v[54:55], v[54:55], v[180:181]
	v_pk_add_f32 v[56:57], v[56:57], v[182:183]
	v_cvt_pk_bf16_f32 v54, v54, v55
	v_cvt_pk_bf16_f32 v55, v56, v57
	global_store_dwordx2 v[240:241], v[54:55], off offset:256
	s_waitcnt vmcnt(27)
	v_pk_add_f32 v[50:51], v[50:51], v[184:185]
	v_pk_add_f32 v[52:53], v[52:53], v[186:187]
	v_cvt_pk_bf16_f32 v50, v50, v51
	v_cvt_pk_bf16_f32 v51, v52, v53
	global_store_dwordx2 v[240:241], v[50:51], off offset:288
	v_lshl_add_u64 v[240:241], v[240:241], 0, s[26:27]
	s_waitcnt vmcnt(23)
	v_pk_add_f32 v[46:47], v[46:47], v[188:189]
	v_pk_add_f32 v[48:49], v[48:49], v[190:191]
	v_cvt_pk_bf16_f32 v46, v46, v47
	v_cvt_pk_bf16_f32 v47, v48, v49
	global_store_dwordx2 v[240:241], v[46:47], off
	s_waitcnt vmcnt(23)
	v_pk_add_f32 v[42:43], v[42:43], v[192:193]
	v_pk_add_f32 v[44:45], v[44:45], v[194:195]
	v_cvt_pk_bf16_f32 v42, v42, v43
	v_cvt_pk_bf16_f32 v43, v44, v45
	global_store_dwordx2 v[240:241], v[42:43], off offset:32
	s_waitcnt vmcnt(23)
	v_pk_add_f32 v[38:39], v[38:39], v[196:197]
	v_pk_add_f32 v[40:41], v[40:41], v[198:199]
	v_cvt_pk_bf16_f32 v38, v38, v39
	v_cvt_pk_bf16_f32 v39, v40, v41
	global_store_dwordx2 v[240:241], v[38:39], off offset:256
	s_waitcnt vmcnt(23)
	v_pk_add_f32 v[34:35], v[34:35], v[200:201]
	v_pk_add_f32 v[36:37], v[36:37], v[202:203]
	v_cvt_pk_bf16_f32 v34, v34, v35
	v_cvt_pk_bf16_f32 v35, v36, v37
	global_store_dwordx2 v[240:241], v[34:35], off offset:288
	v_lshl_add_u64 v[240:241], v[240:241], 0, s[26:27]
	s_waitcnt vmcnt(19)
	v_pk_add_f32 v[30:31], v[30:31], v[204:205]
	v_pk_add_f32 v[32:33], v[32:33], v[206:207]
	v_cvt_pk_bf16_f32 v30, v30, v31
	v_cvt_pk_bf16_f32 v31, v32, v33
	global_store_dwordx2 v[240:241], v[30:31], off
	s_waitcnt vmcnt(19)
	v_pk_add_f32 v[26:27], v[26:27], v[208:209]
	v_pk_add_f32 v[28:29], v[28:29], v[210:211]
	v_cvt_pk_bf16_f32 v26, v26, v27
	v_cvt_pk_bf16_f32 v27, v28, v29
	global_store_dwordx2 v[240:241], v[26:27], off offset:32
	s_waitcnt vmcnt(19)
	v_pk_add_f32 v[22:23], v[22:23], v[212:213]
	v_pk_add_f32 v[24:25], v[24:25], v[214:215]
	v_cvt_pk_bf16_f32 v22, v22, v23
	v_cvt_pk_bf16_f32 v23, v24, v25
	global_store_dwordx2 v[240:241], v[22:23], off offset:256
	s_waitcnt vmcnt(19)
	v_pk_add_f32 v[18:19], v[18:19], v[216:217]
	v_pk_add_f32 v[20:21], v[20:21], v[218:219]
	v_cvt_pk_bf16_f32 v18, v18, v19
	v_cvt_pk_bf16_f32 v19, v20, v21
	global_store_dwordx2 v[240:241], v[18:19], off offset:288
	v_lshl_add_u64 v[240:241], v[240:241], 0, s[26:27]
	s_waitcnt vmcnt(15)
	v_pk_add_f32 v[14:15], v[14:15], v[220:221]
	v_pk_add_f32 v[16:17], v[16:17], v[222:223]
	v_cvt_pk_bf16_f32 v14, v14, v15
	v_cvt_pk_bf16_f32 v15, v16, v17
	global_store_dwordx2 v[240:241], v[14:15], off
	s_waitcnt vmcnt(15)
	v_pk_add_f32 v[10:11], v[10:11], v[224:225]
	v_pk_add_f32 v[12:13], v[12:13], v[226:227]
	v_cvt_pk_bf16_f32 v10, v10, v11
	v_cvt_pk_bf16_f32 v11, v12, v13
	global_store_dwordx2 v[240:241], v[10:11], off offset:32
	s_waitcnt vmcnt(15)
	v_pk_add_f32 v[6:7], v[6:7], v[228:229]
	v_pk_add_f32 v[8:9], v[8:9], v[230:231]
	v_cvt_pk_bf16_f32 v6, v6, v7
	v_cvt_pk_bf16_f32 v7, v8, v9
	global_store_dwordx2 v[240:241], v[6:7], off offset:256
	s_waitcnt vmcnt(15)
	v_pk_add_f32 v[2:3], v[2:3], v[236:237]
	v_pk_add_f32 v[4:5], v[4:5], v[238:239]
	v_cvt_pk_bf16_f32 v2, v2, v3
	v_cvt_pk_bf16_f32 v3, v4, v5
	global_store_dwordx2 v[240:241], v[2:3], off offset:288
	s_mov_b64 s[20:21], -1
	s_cbranch_vccnz .LBB0_1099
	s_andn2_b64 vcc, exec, s[4:5]
	s_cbranch_vccnz .LBB0_1098
	s_barrier
	s_branch .LBB0_1098

; #define LAS __attribute__((address_space(3)))
; DI void phase_ln2(const Args& A, int l, LAS unsigned char* lds, int bid, int G, int tid, int wave, int lane) {
;     ...
;     __syncthreads();
;     { const u32x4_t* src = (const u32x4_t*)(A.ws + WS_WP + (size_t)l * 2 * NE * L2_WLD * 2);
;       for (int i = tid; i < 2 * NE * L2_WLD * 2 / 16; i += NTHR) *(LAS u32x4_t*)(lds + L2_WHI + i * 16) = src[i]; }
;     for (int i = tid; i < DM; i += NTHR) g2s[i] = g2[i];
.LBB0_1164:
	s_cmp_lt_i32 s6, 8
	s_cselect_b64 s[0:1], -1, 0
	s_and_b64 s[2:3], s[0:1], s[2:3]
	s_andn2_b64 vcc, exec, s[2:3]
	s_cbranch_vccnz .LBB0_1177
	s_waitcnt vmcnt(0)
	v_lshlrev_b32_e32 v2, 4, v0
	v_mov_b32_e32 v3, 0
	v_or_b32_e32 v1, 0xfffffe00, v0
	v_add_u32_e32 v4, 0, v2
	v_lshl_add_u64 v[2:3], s[4:5], 0, v[2:3]
	s_mov_b64 s[2:3], 0x100000
	v_lshl_add_u64 v[2:3], v[2:3], 0, s[2:3]
	s_mov_b64 s[2:3], 0
	s_mov_b64 s[4:5], 0x2000
	s_movk_i32 s6, 0xe1f
	v_mov_b32_e32 v5, v1
	s_barrier
	global_load_dwordx4 v[172:175], v[2:3], off
	v_lshl_add_u64 v[2:3], v[2:3], 0, s[4:5]
	global_load_dwordx4 v[176:179], v[2:3], off
	v_lshl_add_u64 v[2:3], v[2:3], 0, s[4:5]
	global_load_dwordx4 v[180:183], v[2:3], off
	v_lshl_add_u64 v[2:3], v[2:3], 0, s[4:5]
	global_load_dwordx4 v[184:187], v[2:3], off
	v_lshl_add_u64 v[2:3], v[2:3], 0, s[4:5]
	global_load_dwordx4 v[188:191], v[2:3], off
	v_lshl_add_u64 v[2:3], v[2:3], 0, s[4:5]
	global_load_dwordx4 v[192:195], v[2:3], off
	v_lshl_add_u64 v[2:3], v[2:3], 0, s[4:5]
	global_load_dwordx4 v[196:199], v[2:3], off
	v_lshl_add_u64 v[2:3], v[2:3], 0, s[4:5]
	global_load_dwordx4 v[200:203], v[2:3], off
	v_lshl_add_u64 v[2:3], v[2:3], 0, s[4:5]
	v_cmp_gt_u32_e32 vcc, 32, v0
	s_and_saveexec_b64 s[8:9], vcc
	global_load_dwordx4 v[204:207], v[2:3], off
	s_mov_b64 exec, s[8:9]
	v_lshlrev_b32_e32 v2, 2, v0
	v_mov_b32_e32 v3, 0
	v_lshl_add_u64 v[2:3], s[62:63], 0, v[2:3]
	global_load_dword v5, v[2:3], off
	global_load_dword v6, v[2:3], off offset:2048
	v_add_u32_e32 v7, 0x10000, v4
	v_add_u32_e32 v8, 0x10200, v147
	s_waitcnt vmcnt(0)
	ds_write_b128 v4, v[172:175] offset:0
	ds_write_b128 v4, v[176:179] offset:8192
	ds_write_b128 v4, v[180:183] offset:16384
	ds_write_b128 v4, v[184:187] offset:24576
	ds_write_b128 v4, v[188:191] offset:32768
	ds_write_b128 v4, v[192:195] offset:40960
	ds_write_b128 v4, v[196:199] offset:49152
	ds_write_b128 v4, v[200:203] offset:57344
	s_and_saveexec_b64 s[8:9], vcc
	ds_write_b128 v7, v[204:207]
	s_mov_b64 exec, s[8:9]
	ds_write_b32 v8, v5
	ds_write_b32 v8, v6 offset:2048
	s_cmpk_gt_i32 s92, 0xff
	s_cbranch_scc1 .LBB0_1176
	v_and_b32_e32 v1, 15, v0
	v_readlane_b32 s7, v235, 8
	s_add_i32 s2, 0, 0x13200
	v_readlane_b32 s5, v235, 52
	s_bfe_u32 s6, s7, 0x10006
	v_lshl_add_u32 v6, v1, 2, s2
	v_lshl_add_u32 v7, v146, 2, s2
	s_lshl_b32 s2, s5, 3
	s_and_b32 s9, s2, 0x1ffffff0
	s_lshl_b32 s4, s6, 9
	s_lshl_b32 s2, s6, 10
	v_readlane_b32 s16, v235, 9
	v_readlane_b32 s17, v235, 10
	s_add_u32 s2, s16, s2
	v_and_b32_e32 v54, 48, v0
	v_mov_b32_e32 v55, 0
	s_addc_u32 s3, s17, 0
	v_lshlrev_b32_e32 v2, 1, v54
	v_mov_b32_e32 v3, v55
	v_lshl_add_u64 v[2:3], s[2:3], 0, v[2:3]
	s_mov_b64 s[2:3], 0x22600000
	v_lshl_add_u64 v[56:57], v[2:3], 0, s[2:3]
	v_mul_u32_u24_e32 v2, 0x408, v1
	v_lshlrev_b32_e32 v9, 1, v2
	v_mbcnt_lo_u32_b32 v2, -1, 0
	v_mbcnt_hi_u32_b32 v10, -1, v2
	v_and_b32_e32 v4, 64, v10
	v_xor_b32_e32 v2, 16, v10
	v_add_u32_e32 v11, 64, v4
	v_cmp_lt_i32_e32 vcc, v2, v11
	s_lshl_b32 s2, s5, 10
	s_xor_b32 s5, s5, 1
	v_cndmask_b32_e32 v2, v10, v2, vcc
	s_add_i32 s8, 0, 0x11200
	s_and_b32 s12, s7, 0xffffffc0
	s_lshl_b32 s7, s5, 10
	v_lshlrev_b32_e32 v64, 2, v2
	v_xor_b32_e32 v2, 32, v10
	s_add_i32 s11, s8, s2
	s_add_i32 s8, s8, s7
	s_lshl_b32 s13, s5, 6
	v_or_b32_e32 v8, s4, v54
	v_cmp_lt_i32_e32 vcc, v2, v11
	s_add_u32 s4, s16, s4
	s_addc_u32 s5, s17, 0
	v_cndmask_b32_e32 v2, v10, v2, vcc
	v_lshlrev_b32_e32 v65, 2, v2
	v_lshl_add_u64 v[2:3], s[4:5], 0, v[54:55]
	s_mov_b64 s[4:5], 0x2a600000
	v_lshl_add_u64 v[58:59], v[2:3], 0, s[4:5]
	v_lshrrev_b32_e32 v2, 2, v0
	v_and_b32_e32 v2, 12, v2
	v_or_b32_e32 v3, v4, v2
	v_lshlrev_b32_e32 v69, 2, v3
	v_xor_b32_e32 v3, 1, v10
	v_cmp_lt_i32_e32 vcc, v3, v11
	s_lshl_b32 s4, s6, 11
	s_add_i32 s4, s4, 0
	v_cndmask_b32_e32 v3, v10, v3, vcc
	v_lshlrev_b32_e32 v70, 2, v3
	v_xor_b32_e32 v3, 2, v10
	v_cmp_lt_i32_e32 vcc, v3, v11
	s_add_i32 s4, s4, 0x10200
	v_lshl_add_u32 v67, v54, 2, s4
	v_cndmask_b32_e32 v3, v10, v3, vcc
	v_lshlrev_b32_e32 v71, 2, v3
	v_xor_b32_e32 v3, 4, v10
	v_cmp_lt_i32_e32 vcc, v3, v11
	v_lshlrev_b32_e32 v54, 13, v1
	s_cmp_eq_u32 s6, 0
	v_cndmask_b32_e32 v3, v10, v3, vcc
	v_lshlrev_b32_e32 v72, 2, v3
	v_xor_b32_e32 v3, 8, v10
	v_lshl_add_u64 v[4:5], s[16:17], 0, v[54:55]
	s_mov_b64 s[6:7], 0x2c600000
	v_cmp_lt_i32_e32 vcc, v3, v11
	v_lshlrev_b32_e32 v66, 4, v146
	s_cselect_b64 s[4:5], -1, 0
	v_lshl_add_u64 v[60:61], v[4:5], 0, s[6:7]
	v_lshlrev_b32_e32 v4, 1, v8
	v_cndmask_b32_e32 v3, v10, v3, vcc
	s_lshl_b32 s6, s92, 6
	v_cmp_gt_u32_e64 s[2:3], 16, v146
	v_add3_u32 v68, 0, v9, v4
	v_lshlrev_b32_e32 v73, 2, v3
	v_or_b32_e32 v74, 4, v69
	v_or_b32_e32 v75, 8, v69
	v_or_b32_e32 v76, 12, v69
	s_add_i32 s9, s6, s9
	s_lshl_b32 s10, s50, 6
	v_add_u32_e32 v77, s11, v66
	v_add_u32_e32 v78, s12, v7
	v_add_u32_e32 v79, s13, v6
	v_mov_b32_e32 v80, 0x358637bd
	s_mov_b32 s11, 0x800000
	s_mov_b32 s12, 0xc3e00000
	s_mov_b32 s13, 0x3fb8aa3b
	s_mov_b32 s14, 0xc2ce8ed0
	s_mov_b32 s15, 0x42b17218
	v_lshlrev_b32_e32 v54, 2, v2
	v_mov_b32_e32 v81, 0x43e00000
	v_mov_b32_e32 v82, 0x7f800000
	s_mov_b32 s16, s92
	v_readlane_b32 s18, v235, 11
	v_readlane_b32 s19, v235, 12
	s_branch .LBB0_1172

; DI void phase_topk(const Args& A, LAS unsigned char* lds, int bid, int G, int tid, int wave, int lane) {
;     ...
;         for (int r = wave; r < CAP; r += NWAVES) { const int s = list[r];
;             if ((s >> 10) == half) { const uint4* src = (const uint4*)(hb + (size_t)(b * SEQ + s) * DM) + lane; uint4* dstp = (uint4*)(xg + (size_t)(slot0 + r) * DM) + lane; dstp[0] = src[0]; } }
.LBB0_1284:
	s_add_i32 s26, s84, s1
	s_mov_b32 s25, 0
	v_mov_b32_e32 v2, s0
	ds_read_b32 v34, v2 offset:0
	ds_read_b32 v35, v2 offset:32
	ds_read_b32 v36, v2 offset:64
	ds_read_b32 v37, v2 offset:96
	ds_read_b32 v38, v2 offset:128
	ds_read_b32 v39, v2 offset:160
	ds_read_b32 v40, v2 offset:192
	ds_read_b32 v41, v2 offset:224
	ds_read_b32 v42, v2 offset:256
	ds_read_b32 v43, v2 offset:288
	ds_read_b32 v44, v2 offset:320
	ds_read_b32 v45, v2 offset:352
	ds_read_b32 v46, v2 offset:384
	ds_read_b32 v47, v2 offset:416
	ds_read_b32 v8, v2 offset:448
	ds_read_b32 v9, v2 offset:480
	s_waitcnt lgkmcnt(0)
	v_add_u32_e32 v4, s85, v34
	v_ashrrev_i32_e32 v5, 31, v4
	v_lshlrev_b64 v[4:5], 10, v[4:5]
	v_lshl_add_u64 v[4:5], v[14:15], 0, v[4:5]
	global_load_dwordx4 v[172:175], v[4:5], off
	v_add_u32_e32 v4, s85, v35
	v_ashrrev_i32_e32 v5, 31, v4
	v_lshlrev_b64 v[4:5], 10, v[4:5]
	v_lshl_add_u64 v[4:5], v[14:15], 0, v[4:5]
	global_load_dwordx4 v[176:179], v[4:5], off
	v_add_u32_e32 v4, s85, v36
	v_ashrrev_i32_e32 v5, 31, v4
	v_lshlrev_b64 v[4:5], 10, v[4:5]
	v_lshl_add_u64 v[4:5], v[14:15], 0, v[4:5]
	global_load_dwordx4 v[180:183], v[4:5], off
	v_add_u32_e32 v4, s85, v37
	v_ashrrev_i32_e32 v5, 31, v4
	v_lshlrev_b64 v[4:5], 10, v[4:5]
	v_lshl_add_u64 v[4:5], v[14:15], 0, v[4:5]
	global_load_dwordx4 v[184:187], v[4:5], off
	v_add_u32_e32 v4, s85, v38
	v_ashrrev_i32_e32 v5, 31, v4
	v_lshlrev_b64 v[4:5], 10, v[4:5]
	v_lshl_add_u64 v[4:5], v[14:15], 0, v[4:5]
	global_load_dwordx4 v[188:191], v[4:5], off
	v_add_u32_e32 v4, s85, v39
	v_ashrrev_i32_e32 v5, 31, v4
	v_lshlrev_b64 v[4:5], 10, v[4:5]
	v_lshl_add_u64 v[4:5], v[14:15], 0, v[4:5]
	global_load_dwordx4 v[192:195], v[4:5], off
	v_add_u32_e32 v4, s85, v40
	v_ashrrev_i32_e32 v5, 31, v4
	v_lshlrev_b64 v[4:5], 10, v[4:5]
	v_lshl_add_u64 v[4:5], v[14:15], 0, v[4:5]
	global_load_dwordx4 v[196:199], v[4:5], off
	v_add_u32_e32 v4, s85, v41
	v_ashrrev_i32_e32 v5, 31, v4
	v_lshlrev_b64 v[4:5], 10, v[4:5]
	v_lshl_add_u64 v[4:5], v[14:15], 0, v[4:5]
	global_load_dwordx4 v[200:203], v[4:5], off
	v_add_u32_e32 v4, s85, v42
	v_ashrrev_i32_e32 v5, 31, v4
	v_lshlrev_b64 v[4:5], 10, v[4:5]
	v_lshl_add_u64 v[4:5], v[14:15], 0, v[4:5]
	global_load_dwordx4 v[204:207], v[4:5], off
	v_add_u32_e32 v4, s85, v43
	v_ashrrev_i32_e32 v5, 31, v4
	v_lshlrev_b64 v[4:5], 10, v[4:5]
	v_lshl_add_u64 v[4:5], v[14:15], 0, v[4:5]
	global_load_dwordx4 v[208:211], v[4:5], off
	v_add_u32_e32 v4, s85, v44
	v_ashrrev_i32_e32 v5, 31, v4
	v_lshlrev_b64 v[4:5], 10, v[4:5]
	v_lshl_add_u64 v[4:5], v[14:15], 0, v[4:5]
	global_load_dwordx4 v[212:215], v[4:5], off
	v_add_u32_e32 v4, s85, v45
	v_ashrrev_i32_e32 v5, 31, v4
	v_lshlrev_b64 v[4:5], 10, v[4:5]
	v_lshl_add_u64 v[4:5], v[14:15], 0, v[4:5]
	global_load_dwordx4 v[216:219], v[4:5], off
	v_add_u32_e32 v4, s85, v46
	v_ashrrev_i32_e32 v5, 31, v4
	v_lshlrev_b64 v[4:5], 10, v[4:5]
	v_lshl_add_u64 v[4:5], v[14:15], 0, v[4:5]
	global_load_dwordx4 v[220:223], v[4:5], off
	v_add_u32_e32 v4, s85, v47
	v_ashrrev_i32_e32 v5, 31, v4
	v_lshlrev_b64 v[4:5], 10, v[4:5]
	v_lshl_add_u64 v[4:5], v[14:15], 0, v[4:5]
	global_load_dwordx4 v[224:227], v[4:5], off
	v_add_u32_e32 v4, s85, v8
	v_ashrrev_i32_e32 v5, 31, v4
	v_lshlrev_b64 v[4:5], 10, v[4:5]
	v_lshl_add_u64 v[4:5], v[14:15], 0, v[4:5]
	global_load_dwordx4 v[228:231], v[4:5], off
	v_add_u32_e32 v4, s85, v9
	v_ashrrev_i32_e32 v5, 31, v4
	v_lshlrev_b64 v[4:5], 10, v[4:5]
	v_lshl_add_u64 v[4:5], v[14:15], 0, v[4:5]
	global_load_dwordx4 v[236:239], v[4:5], off
	s_waitcnt vmcnt(0)
	v_readfirstlane_b32 s27, v34
	s_add_i32 s24, s26, 0
	s_lshl_b32 s24, s24, 10
	s_ashr_i32 s27, s27, 10
	s_cmp_lg_u32 s27, s83
	s_cbranch_scc1 .Lgs0_0
	v_lshl_add_u64 v[6:7], v[16:17], 0, s[24:25]
	global_store_dwordx4 v[6:7], v[172:175], off
.Lgs0_0:
	v_readfirstlane_b32 s27, v35
	s_add_i32 s24, s26, 8
	s_lshl_b32 s24, s24, 10
	s_ashr_i32 s27, s27, 10
	s_cmp_lg_u32 s27, s83
	s_cbranch_scc1 .Lgs0_1
	v_lshl_add_u64 v[6:7], v[16:17], 0, s[24:25]
	global_store_dwordx4 v[6:7], v[176:179], off
.Lgs0_1:
	v_readfirstlane_b32 s27, v36
	s_add_i32 s24, s26, 16
	s_lshl_b32 s24, s24, 10
	s_ashr_i32 s27, s27, 10
	s_cmp_lg_u32 s27, s83
	s_cbranch_scc1 .Lgs0_2
	v_lshl_add_u64 v[6:7], v[16:17], 0, s[24:25]
	global_store_dwordx4 v[6:7], v[180:183], off
.Lgs0_2:
	v_readfirstlane_b32 s27, v37
	s_add_i32 s24, s26, 24
	s_lshl_b32 s24, s24, 10
	s_ashr_i32 s27, s27, 10
	s_cmp_lg_u32 s27, s83
	s_cbranch_scc1 .Lgs0_3
	v_lshl_add_u64 v[6:7], v[16:17], 0, s[24:25]
	global_store_dwordx4 v[6:7], v[184:187], off
.Lgs0_3:
	v_readfirstlane_b32 s27, v38
	s_add_i32 s24, s26, 32
	s_lshl_b32 s24, s24, 10
	s_ashr_i32 s27, s27, 10
	s_cmp_lg_u32 s27, s83
	s_cbranch_scc1 .Lgs0_4
	v_lshl_add_u64 v[6:7], v[16:17], 0, s[24:25]
	global_store_dwordx4 v[6:7], v[188:191], off
.Lgs0_4:
	v_readfirstlane_b32 s27, v39
	s_add_i32 s24, s26, 40
	s_lshl_b32 s24, s24, 10
	s_ashr_i32 s27, s27, 10
	s_cmp_lg_u32 s27, s83
	s_cbranch_scc1 .Lgs0_5
	v_lshl_add_u64 v[6:7], v[16:17], 0, s[24:25]
	global_store_dwordx4 v[6:7], v[192:195], off
.Lgs0_5:
	v_readfirstlane_b32 s27, v40
	s_add_i32 s24, s26, 48
	s_lshl_b32 s24, s24, 10
	s_ashr_i32 s27, s27, 10
	s_cmp_lg_u32 s27, s83
	s_cbranch_scc1 .Lgs0_6
	v_lshl_add_u64 v[6:7], v[16:17], 0, s[24:25]
	global_store_dwordx4 v[6:7], v[196:199], off
.Lgs0_6:
	v_readfirstlane_b32 s27, v41
	s_add_i32 s24, s26, 56
	s_lshl_b32 s24, s24, 10
	s_ashr_i32 s27, s27, 10
	s_cmp_lg_u32 s27, s83
	s_cbranch_scc1 .Lgs0_7
	v_lshl_add_u64 v[6:7], v[16:17], 0, s[24:25]
	global_store_dwordx4 v[6:7], v[200:203], off
; DI void phase_topk(const Args& A, LAS unsigned char* lds, int bid, int G, int tid, int wave, int lane) {
;     ...
;         for (int r = wave; r < CAP; r += NWAVES) { const int s = list[r];
;             if ((s >> 10) == half) { const uint4* src = (const uint4*)(hb + (size_t)(b * SEQ + s) * DM) + lane; uint4* dstp = (uint4*)(xg + (size_t)(slot0 + r) * DM) + lane; dstp[0] = src[0]; } }
.Lgs0_7:
	v_readfirstlane_b32 s27, v42
	s_add_i32 s24, s26, 64
	s_lshl_b32 s24, s24, 10
	s_ashr_i32 s27, s27, 10
	s_cmp_lg_u32 s27, s83
	s_cbranch_scc1 .Lgs0_8
	v_lshl_add_u64 v[6:7], v[16:17], 0, s[24:25]
	global_store_dwordx4 v[6:7], v[204:207], off
.Lgs0_8:
	v_readfirstlane_b32 s27, v43
	s_add_i32 s24, s26, 72
	s_lshl_b32 s24, s24, 10
	s_ashr_i32 s27, s27, 10
	s_cmp_lg_u32 s27, s83
	s_cbranch_scc1 .Lgs0_9
	v_lshl_add_u64 v[6:7], v[16:17], 0, s[24:25]
	global_store_dwordx4 v[6:7], v[208:211], off
.Lgs0_9:
	v_readfirstlane_b32 s27, v44
	s_add_i32 s24, s26, 80
	s_lshl_b32 s24, s24, 10
	s_ashr_i32 s27, s27, 10
	s_cmp_lg_u32 s27, s83
	s_cbranch_scc1 .Lgs0_10
	v_lshl_add_u64 v[6:7], v[16:17], 0, s[24:25]
	global_store_dwordx4 v[6:7], v[212:215], off
.Lgs0_10:
	v_readfirstlane_b32 s27, v45
	s_add_i32 s24, s26, 88
	s_lshl_b32 s24, s24, 10
	s_ashr_i32 s27, s27, 10
	s_cmp_lg_u32 s27, s83
	s_cbranch_scc1 .Lgs0_11
	v_lshl_add_u64 v[6:7], v[16:17], 0, s[24:25]
	global_store_dwordx4 v[6:7], v[216:219], off
.Lgs0_11:
	v_readfirstlane_b32 s27, v46
	s_add_i32 s24, s26, 96
	s_lshl_b32 s24, s24, 10
	s_ashr_i32 s27, s27, 10
	s_cmp_lg_u32 s27, s83
	s_cbranch_scc1 .Lgs0_12
	v_lshl_add_u64 v[6:7], v[16:17], 0, s[24:25]
	global_store_dwordx4 v[6:7], v[220:223], off
.Lgs0_12:
	v_readfirstlane_b32 s27, v47
	s_add_i32 s24, s26, 104
	s_lshl_b32 s24, s24, 10
	s_ashr_i32 s27, s27, 10
	s_cmp_lg_u32 s27, s83
	s_cbranch_scc1 .Lgs0_13
	v_lshl_add_u64 v[6:7], v[16:17], 0, s[24:25]
	global_store_dwordx4 v[6:7], v[224:227], off
.Lgs0_13:
	v_readfirstlane_b32 s27, v8
	s_add_i32 s24, s26, 112
	s_lshl_b32 s24, s24, 10
	s_ashr_i32 s27, s27, 10
	s_cmp_lg_u32 s27, s83
	s_cbranch_scc1 .Lgs0_14
	v_lshl_add_u64 v[6:7], v[16:17], 0, s[24:25]
	global_store_dwordx4 v[6:7], v[228:231], off
.Lgs0_14:
	v_readfirstlane_b32 s27, v9
	s_add_i32 s24, s26, 120
	s_lshl_b32 s24, s24, 10
	s_ashr_i32 s27, s27, 10
	s_cmp_lg_u32 s27, s83
	s_cbranch_scc1 .Lgs0_15
	v_lshl_add_u64 v[6:7], v[16:17], 0, s[24:25]
	global_store_dwordx4 v[6:7], v[236:239], off
.Lgs0_15:
	ds_read_b32 v34, v2 offset:512
	ds_read_b32 v35, v2 offset:544
	ds_read_b32 v36, v2 offset:576
	ds_read_b32 v37, v2 offset:608
	ds_read_b32 v38, v2 offset:640
	ds_read_b32 v39, v2 offset:672
	ds_read_b32 v40, v2 offset:704
	ds_read_b32 v41, v2 offset:736
	ds_read_b32 v42, v2 offset:768
	ds_read_b32 v43, v2 offset:800
	ds_read_b32 v44, v2 offset:832
	ds_read_b32 v45, v2 offset:864
	ds_read_b32 v46, v2 offset:896
	ds_read_b32 v47, v2 offset:928
	ds_read_b32 v8, v2 offset:960
	ds_read_b32 v9, v2 offset:992
	s_waitcnt lgkmcnt(0)
	v_add_u32_e32 v4, s85, v34
	v_ashrrev_i32_e32 v5, 31, v4
	v_lshlrev_b64 v[4:5], 10, v[4:5]
	v_lshl_add_u64 v[4:5], v[14:15], 0, v[4:5]
	global_load_dwordx4 v[172:175], v[4:5], off
	v_add_u32_e32 v4, s85, v35
	v_ashrrev_i32_e32 v5, 31, v4
	v_lshlrev_b64 v[4:5], 10, v[4:5]
	v_lshl_add_u64 v[4:5], v[14:15], 0, v[4:5]
	global_load_dwordx4 v[176:179], v[4:5], off
	v_add_u32_e32 v4, s85, v36
	v_ashrrev_i32_e32 v5, 31, v4
	v_lshlrev_b64 v[4:5], 10, v[4:5]
	v_lshl_add_u64 v[4:5], v[14:15], 0, v[4:5]
	global_load_dwordx4 v[180:183], v[4:5], off
	v_add_u32_e32 v4, s85, v37
	v_ashrrev_i32_e32 v5, 31, v4
	v_lshlrev_b64 v[4:5], 10, v[4:5]
	v_lshl_add_u64 v[4:5], v[14:15], 0, v[4:5]
	global_load_dwordx4 v[184:187], v[4:5], off
	v_add_u32_e32 v4, s85, v38
	v_ashrrev_i32_e32 v5, 31, v4
	v_lshlrev_b64 v[4:5], 10, v[4:5]
	v_lshl_add_u64 v[4:5], v[14:15], 0, v[4:5]
	global_load_dwordx4 v[188:191], v[4:5], off
	v_add_u32_e32 v4, s85, v39
	v_ashrrev_i32_e32 v5, 31, v4
	v_lshlrev_b64 v[4:5], 10, v[4:5]
	v_lshl_add_u64 v[4:5], v[14:15], 0, v[4:5]
	global_load_dwordx4 v[192:195], v[4:5], off
	v_add_u32_e32 v4, s85, v40
	v_ashrrev_i32_e32 v5, 31, v4
	v_lshlrev_b64 v[4:5], 10, v[4:5]
	v_lshl_add_u64 v[4:5], v[14:15], 0, v[4:5]
	global_load_dwordx4 v[196:199], v[4:5], off
	v_add_u32_e32 v4, s85, v41
	v_ashrrev_i32_e32 v5, 31, v4
	v_lshlrev_b64 v[4:5], 10, v[4:5]
	v_lshl_add_u64 v[4:5], v[14:15], 0, v[4:5]
	global_load_dwordx4 v[200:203], v[4:5], off
	v_add_u32_e32 v4, s85, v42
	v_ashrrev_i32_e32 v5, 31, v4
	v_lshlrev_b64 v[4:5], 10, v[4:5]
	v_lshl_add_u64 v[4:5], v[14:15], 0, v[4:5]
	global_load_dwordx4 v[204:207], v[4:5], off
	v_add_u32_e32 v4, s85, v43
	v_ashrrev_i32_e32 v5, 31, v4
	v_lshlrev_b64 v[4:5], 10, v[4:5]
	v_lshl_add_u64 v[4:5], v[14:15], 0, v[4:5]
	global_load_dwordx4 v[208:211], v[4:5], off
	v_add_u32_e32 v4, s85, v44
	v_ashrrev_i32_e32 v5, 31, v4
	v_lshlrev_b64 v[4:5], 10, v[4:5]
	v_lshl_add_u64 v[4:5], v[14:15], 0, v[4:5]
	global_load_dwordx4 v[212:215], v[4:5], off
	v_add_u32_e32 v4, s85, v45
	v_ashrrev_i32_e32 v5, 31, v4
	v_lshlrev_b64 v[4:5], 10, v[4:5]
	v_lshl_add_u64 v[4:5], v[14:15], 0, v[4:5]
	global_load_dwordx4 v[216:219], v[4:5], off
	v_add_u32_e32 v4, s85, v46
	v_ashrrev_i32_e32 v5, 31, v4
	v_lshlrev_b64 v[4:5], 10, v[4:5]
	v_lshl_add_u64 v[4:5], v[14:15], 0, v[4:5]
	global_load_dwordx4 v[220:223], v[4:5], off
	v_add_u32_e32 v4, s85, v47
	v_ashrrev_i32_e32 v5, 31, v4
	v_lshlrev_b64 v[4:5], 10, v[4:5]
	v_lshl_add_u64 v[4:5], v[14:15], 0, v[4:5]
	global_load_dwordx4 v[224:227], v[4:5], off
	v_add_u32_e32 v4, s85, v8
	v_ashrrev_i32_e32 v5, 31, v4
	v_lshlrev_b64 v[4:5], 10, v[4:5]
	v_lshl_add_u64 v[4:5], v[14:15], 0, v[4:5]
	global_load_dwordx4 v[228:231], v[4:5], off
	v_add_u32_e32 v4, s85, v9
	v_ashrrev_i32_e32 v5, 31, v4
	v_lshlrev_b64 v[4:5], 10, v[4:5]
	v_lshl_add_u64 v[4:5], v[14:15], 0, v[4:5]
	global_load_dwordx4 v[236:239], v[4:5], off
	s_waitcnt vmcnt(0)
	v_readfirstlane_b32 s27, v34
	s_add_i32 s24, s26, 128
	s_lshl_b32 s24, s24, 10
	s_ashr_i32 s27, s27, 10
	s_cmp_lg_u32 s27, s83
	s_cbranch_scc1 .Lgs0_16
	v_lshl_add_u64 v[6:7], v[16:17], 0, s[24:25]
	global_store_dwordx4 v[6:7], v[172:175], off
; DI void phase_topk(const Args& A, LAS unsigned char* lds, int bid, int G, int tid, int wave, int lane) {
;     ...
;         for (int r = wave; r < CAP; r += NWAVES) { const int s = list[r];
;             if ((s >> 10) == half) { const uint4* src = (const uint4*)(hb + (size_t)(b * SEQ + s) * DM) + lane; uint4* dstp = (uint4*)(xg + (size_t)(slot0 + r) * DM) + lane; dstp[0] = src[0]; } }
.Lgs0_16:
	v_readfirstlane_b32 s27, v35
	s_add_i32 s24, s26, 136
	s_lshl_b32 s24, s24, 10
	s_ashr_i32 s27, s27, 10
	s_cmp_lg_u32 s27, s83
	s_cbranch_scc1 .Lgs0_17
	v_lshl_add_u64 v[6:7], v[16:17], 0, s[24:25]
	global_store_dwordx4 v[6:7], v[176:179], off
.Lgs0_17:
	v_readfirstlane_b32 s27, v36
	s_add_i32 s24, s26, 144
	s_lshl_b32 s24, s24, 10
	s_ashr_i32 s27, s27, 10
	s_cmp_lg_u32 s27, s83
	s_cbranch_scc1 .Lgs0_18
	v_lshl_add_u64 v[6:7], v[16:17], 0, s[24:25]
	global_store_dwordx4 v[6:7], v[180:183], off
.Lgs0_18:
	v_readfirstlane_b32 s27, v37
	s_add_i32 s24, s26, 152
	s_lshl_b32 s24, s24, 10
	s_ashr_i32 s27, s27, 10
	s_cmp_lg_u32 s27, s83
	s_cbranch_scc1 .Lgs0_19
	v_lshl_add_u64 v[6:7], v[16:17], 0, s[24:25]
	global_store_dwordx4 v[6:7], v[184:187], off
.Lgs0_19:
	v_readfirstlane_b32 s27, v38
	s_add_i32 s24, s26, 160
	s_lshl_b32 s24, s24, 10
	s_ashr_i32 s27, s27, 10
	s_cmp_lg_u32 s27, s83
	s_cbranch_scc1 .Lgs0_20
	v_lshl_add_u64 v[6:7], v[16:17], 0, s[24:25]
	global_store_dwordx4 v[6:7], v[188:191], off
.Lgs0_20:
	v_readfirstlane_b32 s27, v39
	s_add_i32 s24, s26, 168
	s_lshl_b32 s24, s24, 10
	s_ashr_i32 s27, s27, 10
	s_cmp_lg_u32 s27, s83
	s_cbranch_scc1 .Lgs0_21
	v_lshl_add_u64 v[6:7], v[16:17], 0, s[24:25]
	global_store_dwordx4 v[6:7], v[192:195], off
.Lgs0_21:
	v_readfirstlane_b32 s27, v40
	s_add_i32 s24, s26, 176
	s_lshl_b32 s24, s24, 10
	s_ashr_i32 s27, s27, 10
	s_cmp_lg_u32 s27, s83
	s_cbranch_scc1 .Lgs0_22
	v_lshl_add_u64 v[6:7], v[16:17], 0, s[24:25]
	global_store_dwordx4 v[6:7], v[196:199], off
.Lgs0_22:
	v_readfirstlane_b32 s27, v41
	s_add_i32 s24, s26, 184
	s_lshl_b32 s24, s24, 10
	s_ashr_i32 s27, s27, 10
	s_cmp_lg_u32 s27, s83
	s_cbranch_scc1 .Lgs0_23
	v_lshl_add_u64 v[6:7], v[16:17], 0, s[24:25]
	global_store_dwordx4 v[6:7], v[200:203], off
.Lgs0_23:
	v_readfirstlane_b32 s27, v42
	s_add_i32 s24, s26, 192
	s_lshl_b32 s24, s24, 10
	s_ashr_i32 s27, s27, 10
	s_cmp_lg_u32 s27, s83
	s_cbranch_scc1 .Lgs0_24
	v_lshl_add_u64 v[6:7], v[16:17], 0, s[24:25]
	global_store_dwordx4 v[6:7], v[204:207], off
.Lgs0_24:
	v_readfirstlane_b32 s27, v43
	s_add_i32 s24, s26, 200
	s_lshl_b32 s24, s24, 10
	s_ashr_i32 s27, s27, 10
	s_cmp_lg_u32 s27, s83
	s_cbranch_scc1 .Lgs0_25
	v_lshl_add_u64 v[6:7], v[16:17], 0, s[24:25]
	global_store_dwordx4 v[6:7], v[208:211], off
.Lgs0_25:
	v_readfirstlane_b32 s27, v44
	s_add_i32 s24, s26, 208
	s_lshl_b32 s24, s24, 10
	s_ashr_i32 s27, s27, 10
	s_cmp_lg_u32 s27, s83
	s_cbranch_scc1 .Lgs0_26
	v_lshl_add_u64 v[6:7], v[16:17], 0, s[24:25]
	global_store_dwordx4 v[6:7], v[212:215], off
.Lgs0_26:
	v_readfirstlane_b32 s27, v45
	s_add_i32 s24, s26, 216
	s_lshl_b32 s24, s24, 10
	s_ashr_i32 s27, s27, 10
	s_cmp_lg_u32 s27, s83
	s_cbranch_scc1 .Lgs0_27
	v_lshl_add_u64 v[6:7], v[16:17], 0, s[24:25]
	global_store_dwordx4 v[6:7], v[216:219], off
.Lgs0_27:
	v_readfirstlane_b32 s27, v46
	s_add_i32 s24, s26, 224
	s_lshl_b32 s24, s24, 10
	s_ashr_i32 s27, s27, 10
	s_cmp_lg_u32 s27, s83
	s_cbranch_scc1 .Lgs0_28
	v_lshl_add_u64 v[6:7], v[16:17], 0, s[24:25]
	global_store_dwordx4 v[6:7], v[220:223], off
.Lgs0_28:
	v_readfirstlane_b32 s27, v47
	s_add_i32 s24, s26, 232
	s_lshl_b32 s24, s24, 10
	s_ashr_i32 s27, s27, 10
	s_cmp_lg_u32 s27, s83
	s_cbranch_scc1 .Lgs0_29
	v_lshl_add_u64 v[6:7], v[16:17], 0, s[24:25]
	global_store_dwordx4 v[6:7], v[224:227], off
.Lgs0_29:
	v_readfirstlane_b32 s27, v8
	s_add_i32 s24, s26, 240
	s_lshl_b32 s24, s24, 10
	s_ashr_i32 s27, s27, 10
	s_cmp_lg_u32 s27, s83
	s_cbranch_scc1 .Lgs0_30
	v_lshl_add_u64 v[6:7], v[16:17], 0, s[24:25]
	global_store_dwordx4 v[6:7], v[228:231], off
.Lgs0_30:
	v_readfirstlane_b32 s27, v9
	s_add_i32 s24, s26, 248
	s_lshl_b32 s24, s24, 10
	s_ashr_i32 s27, s27, 10
	s_cmp_lg_u32 s27, s83
	s_cbranch_scc1 .Lgs0_31
	v_lshl_add_u64 v[6:7], v[16:17], 0, s[24:25]
	global_store_dwordx4 v[6:7], v[236:239], off
.Lgs0_31:
	s_branch .LBB0_1230

; #define LAS __attribute__((address_space(3)))
; DI void attn_unit(const Args& A, LAS unsigned char* lds, int unit, int tid, int wave, int lane) {
;     const bf16* Z = (const bf16*)(A.ws + WS_Z); bf16* ao = (bf16*)(A.ws + WS_ATTO); float* al = (float*)(A.ws + WS_ATTL);
;     const int x = unit & 15; int r0 = unit >> 4; const int hh = r0 & 3; r0 >>= 2; const int b = r0 % NB, br = r0 / NB;
;     const int dil = br == 0 ? 1 : (br == 1 ? 4 : 16), lsub = SEQ / dil, nblk = lsub / 128;
;     const int res = x / nblk, nbk = x % nblk, l0 = nbk * 128, wbase = l0 - 64;
;     LAS bf16* Qs = (LAS bf16*)(lds + AT_QS); LAS bf16* Ks = (LAS bf16*)(lds + AT_KS); LAS bf16* Vt = (LAS bf16*)(lds + AT_VT); LAS float* btab = (LAS float*)(lds + AT_BT);
;     __syncthreads();
; #pragma unroll
;     for (int i = 0; i < 2; ++i) { const int id = tid + 512 * i, row = id >> 3, ch = id & 7; const int tok = b * SEQ + (l0 + row) * dil + res;
;         *(LAS u32x4_t*)(Qs + row * AT_QLD + ch * 8) = *(const u32x4_t*)(Z + (size_t)tok * ZLD + ZA + hh * 64 + ch * 8); }
;     for (int id = tid; id < 272 * 8; id += NTHR) { const int row = id >> 3, ch = id & 7; const int pos = wbase + row; u32x4_t v = (u32x4_t){0u, 0u, 0u, 0u};
;         if (row < 256 && pos >= 0 && pos < lsub) v = *(const u32x4_t*)(Z + (size_t)(b * SEQ + pos * dil + res) * ZLD + ZA + 256 + hh * 64 + ch * 8);
;         *(LAS u32x4_t*)(Ks + row * AT_QLD + ch * 8) = v; }
;     for (int id = tid; id < 272 * 8; id += NTHR) { const int key = id % 272, ch = id / 272; const int pos = wbase + key; u32x4_t v = (u32x4_t){0u, 0u, 0u, 0u};
;         if (key < 256 && pos >= 0 && pos < lsub) v = *(const u32x4_t*)(Z + (size_t)(b * SEQ + pos * dil + res) * ZLD + ZA + 512 + hh * 64 + ch * 8);
;         LAS bf16* d = Vt + (ch * 8) * AT_VLD + key;
;         d[0] = (bf16)(v.x & 0xffffu); d[AT_VLD] = (bf16)(v.x >> 16); d[2 * AT_VLD] = (bf16)(v.y & 0xffffu); d[3 * AT_VLD] = (bf16)(v.y >> 16);
;         d[4 * AT_VLD] = (bf16)(v.z & 0xffffu); d[5 * AT_VLD] = (bf16)(v.z >> 16); d[6 * AT_VLD] = (bf16)(v.w & 0xffffu); d[7 * AT_VLD] = (bf16)(v.w >> 16); }
;     if (tid < 129) btab[tid] = A.in[I_RELB][t5_bucket((tid - 64) * dil) * 4 + hh] * 1.4426950408889634f;
;     __syncthreads();
.LBB0_1704:
	s_cmp_lt_i32 s6, 14
	s_cselect_b64 s[0:1], -1, 0
	v_writelane_b32 v234, s0, 44
	s_nop 1
	v_writelane_b32 v234, s1, 45
	s_and_b64 s[0:1], s[0:1], s[2:3]
	s_andn2_b64 vcc, exec, s[0:1]
	s_cbranch_vccnz .LBB0_1958
	s_cmpk_gt_i32 s50, 0xa0
	s_cselect_b32 s0, 0x600, 0
	s_add_i32 s33, s0, s92
	s_cmpk_gt_i32 s33, 0x5ff
	s_mov_b32 s3, 0
	s_cbranch_scc1 .LBB0_1796
	s_mov_b32 s6, s33
	s_mov_b32 s7, s50
	s_movk_i32 s8, 0x600
	v_readlane_b32 s9, v235, 52
	v_readlane_b32 s2, v235, 9
	v_readlane_b32 s3, v235, 10
	v_readlane_b32 s4, v235, 19
	v_readlane_b32 s5, v235, 20
	s_mov_b32 s72, 0x3e38aa3b
	s_mov_b32 s73, 0x3e38aa3b
	v_lshrrev_b32_e32 v2, 3, v0
	v_and_b32_e32 v3, 7, v0
	v_lshlrev_b32_e32 v3, 4, v3
	s_movk_i32 s39, 0x90
	v_mad_u32_u24 v1, v2, s39, v3
	v_and_b32_e32 v5, 0xff, v0
	v_lshrrev_b32_e32 v6, 8, v0
	s_movk_i32 s39, 0x1180
	v_mul_u32_u24_e32 v4, s39, v6
	v_lshl_add_u32 v4, v5, 1, v4
	v_add_u32_e32 v4, 0xe100, v4
	v_lshlrev_b32_e32 v6, 4, v6
	v_lshlrev_b32_e32 v8, 2, v5
	v_add_u32_e32 v8, 0x16d00, v8
	v_subrev_u32_e32 v165, 16, v0
	s_movk_i32 s39, 0x81
	v_cmp_gt_u32_e64 s[42:43], s39, v165
	s_movk_i32 s39, 0xa0
	v_cmp_gt_u32_e64 s[48:49], s39, v0
	v_cmp_gt_u32_e64 s[46:47], 64, v0
	v_cmp_gt_u32_e64 s[44:45], 16, v146
	v_subrev_u32_e32 v165, 0x50, v0
	v_cmp_lt_i32_e32 vcc, 0, v165
	v_mov_b32_e32 v7, 0
	s_nop 0
	v_cndmask_b32_e64 v166, 0, 16, vcc
	v_lshlrev_b32_e32 v167, 0, v165
	v_sub_u32_e32 v168, 0, v167
	v_max_i32_e32 v167, v167, v168
	v_cvt_f32_u32_e32 v168, v167
	v_mul_f32_e32 v168, 0x3e000000, v168
	v_max_f32_e32 v168, 1.0, v168
	v_log_f32_e32 v168, v168
	v_cmp_gt_u32_e32 vcc, 8, v167
	v_mul_f32_e32 v168, 0x3f924925, v168
	v_cvt_i32_f32_e32 v168, v168
	v_min_i32_e32 v168, 7, v168
	v_add_u32_e32 v168, 8, v168
	v_cndmask_b32_e32 v168, v168, v167, vcc
	v_add_u32_e32 v168, v168, v166
	v_lshl_or_b32 v7, v168, 0, v7
	v_lshlrev_b32_e32 v167, 2, v165
	v_sub_u32_e32 v168, 0, v167
	v_max_i32_e32 v167, v167, v168
	v_cvt_f32_u32_e32 v168, v167
	v_mul_f32_e32 v168, 0x3e000000, v168
	v_max_f32_e32 v168, 1.0, v168
	v_log_f32_e32 v168, v168
	v_cmp_gt_u32_e32 vcc, 8, v167
	v_mul_f32_e32 v168, 0x3f924925, v168
	v_cvt_i32_f32_e32 v168, v168
	v_min_i32_e32 v168, 7, v168
	v_add_u32_e32 v168, 8, v168
	v_cndmask_b32_e32 v168, v168, v167, vcc
	v_add_u32_e32 v168, v168, v166
	v_lshl_or_b32 v7, v168, 8, v7
	v_lshlrev_b32_e32 v167, 4, v165
	v_sub_u32_e32 v168, 0, v167
	v_max_i32_e32 v167, v167, v168
	v_cvt_f32_u32_e32 v168, v167
	v_mul_f32_e32 v168, 0x3e000000, v168
	v_max_f32_e32 v168, 1.0, v168
	v_log_f32_e32 v168, v168
	v_cmp_gt_u32_e32 vcc, 8, v167
	v_mul_f32_e32 v168, 0x3f924925, v168
	v_cvt_i32_f32_e32 v168, v168
	v_min_i32_e32 v168, 7, v168
	v_add_u32_e32 v168, 8, v168
	v_cndmask_b32_e32 v168, v168, v167, vcc
	v_add_u32_e32 v168, v168, v166
	v_lshl_or_b32 v7, v168, 16, v7
	v_and_b32_e32 v165, 15, v146
	v_lshrrev_b32_e32 v166, 4, v146
	s_lshl_b32 s39, s9, 4
	v_add_u32_e32 v40, s39, v165
	s_movk_i32 s40, 0x90
	v_mul_u32_u24_e32 v34, s40, v40
	v_lshl_add_u32 v34, v166, 4, v34
	v_lshlrev_b32_e32 v167, 2, v166
	v_sub_u32_e32 v35, v167, v165
	v_lshlrev_b32_e32 v35, 2, v35
	v_add_u32_e32 v35, 0x16d40, v35
	v_add_u32_e32 v167, s39, v167
	v_lshlrev_b32_e32 v36, 2, v167
	v_add_u32_e32 v36, 0x16f80, v36
	s_movk_i32 s40, 0x230
	v_mul_u32_u24_e32 v37, s40, v165
	v_lshl_add_u32 v37, v167, 1, v37
	v_add_u32_e32 v37, 0xe100, v37
	v_add_u32_e32 v9, 0x2300, v37
	v_add_u32_e32 v118, 0x4600, v37
	v_add_u32_e32 v144, 0x6900, v37
	v_xor_b32_e32 v38, 16, v146
	v_lshlrev_b32_e32 v38, 2, v38
	v_xor_b32_e32 v39, 32, v146
	v_lshlrev_b32_e32 v39, 2, v39
	v_lshlrev_b32_e32 v41, 3, v166
	v_mov_b32_e32 v232, 0
	v_mov_b32_e32 v233, 0
	s_movk_i32 s40, 0x230
	v_mul_u32_u24_e32 v168, s40, v0
	v_add_u32_e32 v168, 0xe300, v168
	s_and_saveexec_b64 s[40:41], s[46:47]
	ds_write_b64 v168, v[232:233] offset:0
	ds_write_b64 v168, v[232:233] offset:8
	ds_write_b64 v168, v[232:233] offset:16
	ds_write_b64 v168, v[232:233] offset:24
	s_mov_b64 exec, s[40:41]
	s_and_b32 s39, s6, 15
	s_bfe_u32 s40, s6, 0x20004
	s_bfe_u32 s41, s6, 0x30006
	s_lshr_b32 s74, s6, 9
	s_lshl_b32 s75, s74, 1
	s_add_i32 s16, s75, 13
	s_add_i32 s20, s75, 9
	s_add_i32 s26, s75, 4
	s_lshl_b32 s28, s74, 3
	s_lshr_b32 s29, 0x800, s75
	s_add_i32 s17, s29, -1
	s_sub_i32 s76, 4, s75
	s_lshr_b32 s77, s39, s76
	s_lshr_b32 s78, 16, s75
	s_add_i32 s78, s78, -1
	s_and_b32 s78, s39, s78
	s_lshl_b32 s19, s78, 7
	s_add_i32 s18, s19, 0xffffffc0
	s_lshl_b32 s79, s41, 11
	s_add_i32 s79, s79, s77
	s_lshl_b32 s80, s40, 7
	s_lshl_b32 s27, s40, 2
	s_lshl_b32 s81, s79, 13
	s_add_u32 s81, s81, s80
	s_add_u32 s81, s81, 0x2ca00000
	s_add_u32 s10, s2, s81
	s_addc_u32 s11, s3, 0
	s_lshl_b32 s82, s74, 14
	s_add_i32 s82, s82, s79
	s_lshl_b32 s83, s82, 9
	s_add_u32 s83, s83, s80
	s_add_u32 s83, s83, 0x34a00000
	s_add_u32 s12, s2, s83
	s_addc_u32 s13, s3, 0
	s_lshl_b32 s84, s82, 4
	s_add_u32 s84, s84, s27
	s_add_u32 s84, s84, 0x36200000
	s_add_u32 s14, s2, s84
	s_addc_u32 s15, s3, 0
	v_add_u32_e32 v165, s19, v2
	v_lshl_add_u32 v165, v165, s16, v3
	s_lshl_b32 s85, 64, s16
	global_load_dwordx4 v[120:123], v165, s[10:11]
	v_add_u32_e32 v166, s85, v165
	global_load_dwordx4 v[124:127], v166, s[10:11]
	v_add_u32_e32 v167, s18, v2
	v_med3_i32 v168, v167, 0, s17
	v_lshl_add_u32 v168, v168, s16, v3
	global_load_dwordx4 v[128:131], v168, s[10:11] offset:512
	v_add_u32_e32 v168, 64, v167
	v_med3_i32 v168, v168, 0, s17
	v_lshl_add_u32 v168, v168, s16, v3
	global_load_dwordx4 v[132:135], v168, s[10:11] offset:512
	v_add_u32_e32 v168, 0x80, v167
	v_med3_i32 v168, v168, 0, s17
	v_lshl_add_u32 v168, v168, s16, v3
	global_load_dwordx4 v[136:139], v168, s[10:11] offset:512
	v_add_u32_e32 v168, 0xc0, v167
	v_med3_i32 v168, v168, 0, s17
	v_lshl_add_u32 v168, v168, s16, v3
	global_load_dwordx4 v[140:143], v168, s[10:11] offset:512
	v_add_u32_e32 v169, s18, v5
	v_med3_i32 v169, v169, 0, s17
	v_lshl_add_u32 v169, v169, s16, v6
	global_load_dwordx4 v[148:151], v169, s[10:11] offset:1024
	global_load_dwordx4 v[152:155], v169, s[10:11] offset:1056
	global_load_dwordx4 v[156:159], v169, s[10:11] offset:1088
	global_load_dwordx4 v[160:163], v169, s[10:11] offset:1120
	v_bfe_u32 v171, v7, s28, 8
	v_lshl_add_u32 v171, v171, 4, s27
	s_mov_b64 exec, s[42:43]
	global_load_dword v164, v171, s[4:5]
	s_mov_b64 exec, -1

; DI void attn_unit(const Args& A, LAS unsigned char* lds, int unit, int tid, int wave, int lane) {
;     const bf16* Z = (const bf16*)(A.ws + WS_Z); bf16* ao = (bf16*)(A.ws + WS_ATTO); float* al = (float*)(A.ws + WS_ATTL);
;     const int x = unit & 15; int r0 = unit >> 4; const int hh = r0 & 3; r0 >>= 2; const int b = r0 % NB, br = r0 / NB;
;     const int dil = br == 0 ? 1 : (br == 1 ? 4 : 16), lsub = SEQ / dil, nblk = lsub / 128;
;     const int res = x / nblk, nbk = x % nblk, l0 = nbk * 128, wbase = l0 - 64;
;     LAS bf16* Qs = (LAS bf16*)(lds + AT_QS); LAS bf16* Ks = (LAS bf16*)(lds + AT_KS); LAS bf16* Vt = (LAS bf16*)(lds + AT_VT); LAS float* btab = (LAS float*)(lds + AT_BT);
;     __syncthreads();
; #pragma unroll
;     for (int i = 0; i < 2; ++i) { const int id = tid + 512 * i, row = id >> 3, ch = id & 7; const int tok = b * SEQ + (l0 + row) * dil + res;
;         *(LAS u32x4_t*)(Qs + row * AT_QLD + ch * 8) = *(const u32x4_t*)(Z + (size_t)tok * ZLD + ZA + hh * 64 + ch * 8); }
;     for (int id = tid; id < 272 * 8; id += NTHR) { const int row = id >> 3, ch = id & 7; const int pos = wbase + row; u32x4_t v = (u32x4_t){0u, 0u, 0u, 0u};
;         if (row < 256 && pos >= 0 && pos < lsub) v = *(const u32x4_t*)(Z + (size_t)(b * SEQ + pos * dil + res) * ZLD + ZA + 256 + hh * 64 + ch * 8);
;         *(LAS u32x4_t*)(Ks + row * AT_QLD + ch * 8) = v; }
;     for (int id = tid; id < 272 * 8; id += NTHR) { const int key = id % 272, ch = id / 272; const int pos = wbase + key; u32x4_t v = (u32x4_t){0u, 0u, 0u, 0u};
;         if (key < 256 && pos >= 0 && pos < lsub) v = *(const u32x4_t*)(Z + (size_t)(b * SEQ + pos * dil + res) * ZLD + ZA + 512 + hh * 64 + ch * 8);
;         LAS bf16* d = Vt + (ch * 8) * AT_VLD + key;
;         d[0] = (bf16)(v.x & 0xffffu); d[AT_VLD] = (bf16)(v.x >> 16); d[2 * AT_VLD] = (bf16)(v.y & 0xffffu); d[3 * AT_VLD] = (bf16)(v.y >> 16);
;         d[4 * AT_VLD] = (bf16)(v.z & 0xffffu); d[5 * AT_VLD] = (bf16)(v.z >> 16); d[6 * AT_VLD] = (bf16)(v.w & 0xffffu); d[7 * AT_VLD] = (bf16)(v.w >> 16); }
;     if (tid < 129) btab[tid] = A.in[I_RELB][t5_bucket((tid - 64) * dil) * 4 + hh] * 1.4426950408889634f;
;     __syncthreads();
; template <int l> DI void run_layer(const Args& A, LAS unsigned char* lds, const XcdBarrier& bar, int lo, int hi, int G, int bid, int tid, int lane, int wave, int gw, int ngw, int gtid, int nthr) {
;     ...
;     PH(3,
.LBB0_2008:
	s_cmp_lt_i32 s6, 15
	s_cselect_b64 s[24:25], -1, 0
	s_and_b64 s[0:1], s[24:25], s[0:1]
	s_andn2_b64 vcc, exec, s[0:1]
	s_cbranch_vccnz .LBB0_2420
	s_cmpk_lt_i32 s50, 0xa1
	s_cselect_b64 s[0:1], -1, 0
	s_cmpk_lt_i32 s92, 0xa0
	s_cselect_b64 s[2:3], -1, 0
	s_or_b64 s[0:1], s[2:3], s[0:1]
	s_and_b64 vcc, exec, s[0:1]
	s_cbranch_vccnz .LBB0_2102
	s_add_i32 s33, s92, 0xffffff60
	s_cmpk_gt_u32 s33, 0x23f
	s_cbranch_scc1 .LBB0_2101
	s_mov_b32 s6, s33
	s_add_i32 s7, s50, 0xffffff60
	s_movk_i32 s8, 0x600
	v_readlane_b32 s9, v235, 52
	v_readlane_b32 s2, v235, 9
	v_readlane_b32 s3, v235, 10
	v_readlane_b32 s4, v235, 19
	v_readlane_b32 s5, v235, 20
	s_mov_b32 s72, 0x3e38aa3b
	s_mov_b32 s73, 0x3e38aa3b
	v_lshrrev_b32_e32 v2, 3, v0
	v_and_b32_e32 v3, 7, v0
	v_lshlrev_b32_e32 v3, 4, v3
	s_movk_i32 s39, 0x90
	v_mad_u32_u24 v1, v2, s39, v3
	v_and_b32_e32 v5, 0xff, v0
	v_lshrrev_b32_e32 v6, 8, v0
	s_movk_i32 s39, 0x1180
	v_mul_u32_u24_e32 v4, s39, v6
	v_lshl_add_u32 v4, v5, 1, v4
	v_add_u32_e32 v4, 0xe100, v4
	v_lshlrev_b32_e32 v6, 4, v6
	v_lshlrev_b32_e32 v8, 2, v5
	v_add_u32_e32 v8, 0x16d00, v8
	v_subrev_u32_e32 v165, 16, v0
	s_movk_i32 s39, 0x81
	v_cmp_gt_u32_e64 s[42:43], s39, v165
	s_movk_i32 s39, 0xa0
	v_cmp_gt_u32_e64 s[48:49], s39, v0
	v_cmp_gt_u32_e64 s[46:47], 64, v0
	v_cmp_gt_u32_e64 s[44:45], 16, v146
	v_subrev_u32_e32 v165, 0x50, v0
	v_cmp_lt_i32_e32 vcc, 0, v165
	v_mov_b32_e32 v7, 0
	s_nop 0
	v_cndmask_b32_e64 v166, 0, 16, vcc
	v_lshlrev_b32_e32 v167, 0, v165
	v_sub_u32_e32 v168, 0, v167
	v_max_i32_e32 v167, v167, v168
	v_cvt_f32_u32_e32 v168, v167
	v_mul_f32_e32 v168, 0x3e000000, v168
	v_max_f32_e32 v168, 1.0, v168
	v_log_f32_e32 v168, v168
	v_cmp_gt_u32_e32 vcc, 8, v167
	v_mul_f32_e32 v168, 0x3f924925, v168
	v_cvt_i32_f32_e32 v168, v168
	v_min_i32_e32 v168, 7, v168
	v_add_u32_e32 v168, 8, v168
	v_cndmask_b32_e32 v168, v168, v167, vcc
	v_add_u32_e32 v168, v168, v166
	v_lshl_or_b32 v7, v168, 0, v7
	v_lshlrev_b32_e32 v167, 2, v165
	v_sub_u32_e32 v168, 0, v167
	v_max_i32_e32 v167, v167, v168
	v_cvt_f32_u32_e32 v168, v167
	v_mul_f32_e32 v168, 0x3e000000, v168
	v_max_f32_e32 v168, 1.0, v168
	v_log_f32_e32 v168, v168
	v_cmp_gt_u32_e32 vcc, 8, v167
	v_mul_f32_e32 v168, 0x3f924925, v168
	v_cvt_i32_f32_e32 v168, v168
	v_min_i32_e32 v168, 7, v168
	v_add_u32_e32 v168, 8, v168
	v_cndmask_b32_e32 v168, v168, v167, vcc
	v_add_u32_e32 v168, v168, v166
	v_lshl_or_b32 v7, v168, 8, v7
	v_lshlrev_b32_e32 v167, 4, v165
	v_sub_u32_e32 v168, 0, v167
	v_max_i32_e32 v167, v167, v168
	v_cvt_f32_u32_e32 v168, v167
	v_mul_f32_e32 v168, 0x3e000000, v168
	v_max_f32_e32 v168, 1.0, v168
	v_log_f32_e32 v168, v168
	v_cmp_gt_u32_e32 vcc, 8, v167
	v_mul_f32_e32 v168, 0x3f924925, v168
	v_cvt_i32_f32_e32 v168, v168
	v_min_i32_e32 v168, 7, v168
	v_add_u32_e32 v168, 8, v168
	v_cndmask_b32_e32 v168, v168, v167, vcc
	v_add_u32_e32 v168, v168, v166
	v_lshl_or_b32 v7, v168, 16, v7
	v_and_b32_e32 v165, 15, v146
	v_lshrrev_b32_e32 v166, 4, v146
	s_lshl_b32 s39, s9, 4
	v_add_u32_e32 v40, s39, v165
	s_movk_i32 s40, 0x90
	v_mul_u32_u24_e32 v34, s40, v40
	v_lshl_add_u32 v34, v166, 4, v34
	v_lshlrev_b32_e32 v167, 2, v166
	v_sub_u32_e32 v35, v167, v165
	v_lshlrev_b32_e32 v35, 2, v35
	v_add_u32_e32 v35, 0x16d40, v35
	v_add_u32_e32 v167, s39, v167
	v_lshlrev_b32_e32 v36, 2, v167
	v_add_u32_e32 v36, 0x16f80, v36
	s_movk_i32 s40, 0x230
	v_mul_u32_u24_e32 v37, s40, v165
	v_lshl_add_u32 v37, v167, 1, v37
	v_add_u32_e32 v37, 0xe100, v37
	v_add_u32_e32 v9, 0x2300, v37
	v_add_u32_e32 v118, 0x4600, v37
	v_add_u32_e32 v144, 0x6900, v37
	v_xor_b32_e32 v38, 16, v146
	v_lshlrev_b32_e32 v38, 2, v38
	v_xor_b32_e32 v39, 32, v146
	v_lshlrev_b32_e32 v39, 2, v39
	v_lshlrev_b32_e32 v41, 3, v166
	v_mov_b32_e32 v232, 0
	v_mov_b32_e32 v233, 0
	s_movk_i32 s40, 0x230
	v_mul_u32_u24_e32 v168, s40, v0
	v_add_u32_e32 v168, 0xe300, v168
	s_and_saveexec_b64 s[40:41], s[46:47]
	ds_write_b64 v168, v[232:233] offset:0
	ds_write_b64 v168, v[232:233] offset:8
	ds_write_b64 v168, v[232:233] offset:16
	ds_write_b64 v168, v[232:233] offset:24
	s_mov_b64 exec, s[40:41]
	s_and_b32 s39, s6, 15
	s_bfe_u32 s40, s6, 0x20004
	s_bfe_u32 s41, s6, 0x30006
	s_lshr_b32 s74, s6, 9
	s_lshl_b32 s75, s74, 1
	s_add_i32 s16, s75, 13
	s_add_i32 s20, s75, 9
	s_add_i32 s26, s75, 4
	s_lshl_b32 s28, s74, 3
	s_lshr_b32 s29, 0x800, s75
	s_add_i32 s17, s29, -1
	s_sub_i32 s76, 4, s75
	s_lshr_b32 s77, s39, s76
	s_lshr_b32 s78, 16, s75
	s_add_i32 s78, s78, -1
	s_and_b32 s78, s39, s78
	s_lshl_b32 s19, s78, 7
	s_add_i32 s18, s19, 0xffffffc0
	s_lshl_b32 s79, s41, 11
	s_add_i32 s79, s79, s77
	s_lshl_b32 s80, s40, 7
	s_lshl_b32 s27, s40, 2
	s_lshl_b32 s81, s79, 13
	s_add_u32 s81, s81, s80
	s_add_u32 s81, s81, 0x2ca00000
	s_add_u32 s10, s2, s81
	s_addc_u32 s11, s3, 0
	s_lshl_b32 s82, s74, 14
	s_add_i32 s82, s82, s79
	s_lshl_b32 s83, s82, 9
	s_add_u32 s83, s83, s80
	s_add_u32 s83, s83, 0x34a00000
	s_add_u32 s12, s2, s83
	s_addc_u32 s13, s3, 0
	s_lshl_b32 s84, s82, 4
	s_add_u32 s84, s84, s27
	s_add_u32 s84, s84, 0x36200000
	s_add_u32 s14, s2, s84
	s_addc_u32 s15, s3, 0
	v_add_u32_e32 v165, s19, v2
	v_lshl_add_u32 v165, v165, s16, v3
	s_lshl_b32 s85, 64, s16
	global_load_dwordx4 v[120:123], v165, s[10:11]
	v_add_u32_e32 v166, s85, v165
	global_load_dwordx4 v[124:127], v166, s[10:11]
	v_add_u32_e32 v167, s18, v2
	v_med3_i32 v168, v167, 0, s17
	v_lshl_add_u32 v168, v168, s16, v3
	global_load_dwordx4 v[128:131], v168, s[10:11] offset:512
	v_add_u32_e32 v168, 64, v167
	v_med3_i32 v168, v168, 0, s17
	v_lshl_add_u32 v168, v168, s16, v3
	global_load_dwordx4 v[132:135], v168, s[10:11] offset:512
	v_add_u32_e32 v168, 0x80, v167
	v_med3_i32 v168, v168, 0, s17
	v_lshl_add_u32 v168, v168, s16, v3
	global_load_dwordx4 v[136:139], v168, s[10:11] offset:512
	v_add_u32_e32 v168, 0xc0, v167
	v_med3_i32 v168, v168, 0, s17
	v_lshl_add_u32 v168, v168, s16, v3
	global_load_dwordx4 v[140:143], v168, s[10:11] offset:512
	v_add_u32_e32 v169, s18, v5
	v_med3_i32 v169, v169, 0, s17
	v_lshl_add_u32 v169, v169, s16, v6
	global_load_dwordx4 v[148:151], v169, s[10:11] offset:1024
	global_load_dwordx4 v[152:155], v169, s[10:11] offset:1056
	global_load_dwordx4 v[156:159], v169, s[10:11] offset:1088
	global_load_dwordx4 v[160:163], v169, s[10:11] offset:1120
	v_bfe_u32 v171, v7, s28, 8
	v_lshl_add_u32 v171, v171, 4, s27
	s_mov_b64 exec, s[42:43]
	global_load_dword v164, v171, s[4:5]
	s_mov_b64 exec, -1

; #define LAS __attribute__((address_space(3)))
; DI void phase_yasm(const Args& A, int l, LAS unsigned char* lds, int gw, int ngw, int tid, int lane) {
;     ...
;     LAS bf16* G2T = (LAS bf16*)lds;
;     __syncthreads();
;     { const u32x4_t* src = (const u32x4_t*)(A.ws + WS_G2T + (size_t)l * RW * 128 * 2);
;       for (int idx = tid; idx < RW * 16; idx += NTHR) { const int col = idx >> 4, ch = idx & 15; *(LAS u32x4_t*)(G2T + col * YA_G2LD + ch * 8) = src[idx]; } }
;     __syncthreads();
.LBB0_2470:
	s_cmp_lt_i32 s6, 16
	s_cselect_b64 s[2:3], -1, 0
	s_and_b64 s[0:1], s[2:3], s[0:1]
	s_andn2_b64 vcc, exec, s[0:1]
	s_cbranch_vccnz .LBB0_2502
	s_waitcnt vmcnt(0)
	v_lshlrev_b32_e32 v2, 4, v0
	v_mov_b32_e32 v3, 0
	v_and_b32_e32 v1, 15, v0
	v_lshl_add_u64 v[2:3], s[4:5], 0, v[2:3]
	s_mov_b64 s[0:1], 0x2c918000
	v_mul_u32_u24_e32 v5, 0x110, v170
	v_lshlrev_b32_e32 v6, 4, v1
	v_or_b32_e32 v4, 0xfffffe00, v0
	v_lshl_add_u64 v[2:3], v[2:3], 0, s[0:1]
	v_add3_u32 v5, v5, v6, 0
	s_mov_b64 s[0:1], 0
	s_mov_b64 s[4:5], 0x2000
	s_movk_i32 s6, 0x15ff
	s_waitcnt lgkmcnt(0)
	s_barrier
	global_load_dwordx4 v[172:175], v[2:3], off
	v_lshl_add_u64 v[2:3], v[2:3], 0, s[4:5]
	global_load_dwordx4 v[176:179], v[2:3], off
	v_lshl_add_u64 v[2:3], v[2:3], 0, s[4:5]
	global_load_dwordx4 v[180:183], v[2:3], off
	v_lshl_add_u64 v[2:3], v[2:3], 0, s[4:5]
	global_load_dwordx4 v[184:187], v[2:3], off
	v_lshl_add_u64 v[2:3], v[2:3], 0, s[4:5]
	global_load_dwordx4 v[188:191], v[2:3], off
	v_lshl_add_u64 v[2:3], v[2:3], 0, s[4:5]
	global_load_dwordx4 v[192:195], v[2:3], off
	v_lshl_add_u64 v[2:3], v[2:3], 0, s[4:5]
	global_load_dwordx4 v[196:199], v[2:3], off
	v_lshl_add_u64 v[2:3], v[2:3], 0, s[4:5]
	global_load_dwordx4 v[200:203], v[2:3], off
	v_lshl_add_u64 v[2:3], v[2:3], 0, s[4:5]
	global_load_dwordx4 v[204:207], v[2:3], off
	v_lshl_add_u64 v[2:3], v[2:3], 0, s[4:5]
	global_load_dwordx4 v[208:211], v[2:3], off
	v_lshl_add_u64 v[2:3], v[2:3], 0, s[4:5]
	global_load_dwordx4 v[212:215], v[2:3], off
	v_lshl_add_u64 v[2:3], v[2:3], 0, s[4:5]
	global_load_dwordx4 v[216:219], v[2:3], off
	v_add_u32_e32 v4, 0x11000, v5
	s_waitcnt vmcnt(0)
	ds_write_b128 v5, v[172:175] offset:0
	ds_write_b128 v5, v[176:179] offset:8704
	ds_write_b128 v5, v[180:183] offset:17408
	ds_write_b128 v5, v[184:187] offset:26112
	ds_write_b128 v5, v[188:191] offset:34816
	ds_write_b128 v5, v[192:195] offset:43520
	ds_write_b128 v5, v[196:199] offset:52224
	ds_write_b128 v5, v[200:203] offset:60928
	ds_write_b128 v4, v[204:207] offset:0
	ds_write_b128 v4, v[208:211] offset:8704
	ds_write_b128 v4, v[212:215] offset:17408
	ds_write_b128 v4, v[216:219] offset:26112
	v_readlane_b32 s4, v235, 9
	v_readlane_b32 s5, v235, 10
	s_add_u32 s18, s4, 0x2ca00000
	s_addc_u32 s19, s5, 0
	s_add_u32 s16, s4, 0x2a600000
	s_addc_u32 s17, s5, 0
	v_readlane_b32 s0, v235, 54
	v_readlane_b32 s6, v235, 11
	v_readlane_b32 s7, v235, 12
	s_cmpk_gt_i32 s0, 0x17ff
	s_waitcnt lgkmcnt(0)
	s_barrier
	v_readlane_b32 s1, v235, 55
	s_cbranch_scc0 .LBB0_2475
	v_lshlrev_b32_e32 v114, 2, v146
	v_lshrrev_b32_e32 v117, 4, v146
	v_and_b32_e32 v121, 3, v0
	s_cbranch_execz .LBB0_2476
	s_branch .LBB0_2483

; #define LAS __attribute__((address_space(3)))
; DI void phase_ln2(const Args& A, int l, LAS unsigned char* lds, int bid, int G, int tid, int wave, int lane) {
;     ...
;     __syncthreads();
;     { const u32x4_t* src = (const u32x4_t*)(A.ws + WS_WP + (size_t)l * 2 * NE * L2_WLD * 2);
;       for (int i = tid; i < 2 * NE * L2_WLD * 2 / 16; i += NTHR) *(LAS u32x4_t*)(lds + L2_WHI + i * 16) = src[i]; }
;     for (int i = tid; i < DM; i += NTHR) g2s[i] = g2[i];
.LBB0_2627:
	s_cmp_lt_i32 s6, 18
	s_cselect_b64 s[2:3], -1, 0
	s_and_b64 s[0:1], s[2:3], s[0:1]
	s_andn2_b64 vcc, exec, s[0:1]
	s_cbranch_vccnz .LBB0_2640
	s_waitcnt vmcnt(0)
	v_lshlrev_b32_e32 v2, 4, v0
	v_mov_b32_e32 v3, 0
	v_or_b32_e32 v1, 0xfffffe00, v0
	v_add_u32_e32 v4, 0, v2
	v_lshl_add_u64 v[2:3], s[4:5], 0, v[2:3]
	s_mov_b64 s[0:1], 0x110200
	v_lshl_add_u64 v[2:3], v[2:3], 0, s[0:1]
	s_mov_b64 s[0:1], 0
	s_mov_b64 s[4:5], 0x2000
	s_movk_i32 s6, 0xe1f
	v_mov_b32_e32 v5, v1
	s_waitcnt lgkmcnt(0)
	s_barrier
	global_load_dwordx4 v[172:175], v[2:3], off
	v_lshl_add_u64 v[2:3], v[2:3], 0, s[4:5]
	global_load_dwordx4 v[176:179], v[2:3], off
	v_lshl_add_u64 v[2:3], v[2:3], 0, s[4:5]
	global_load_dwordx4 v[180:183], v[2:3], off
	v_lshl_add_u64 v[2:3], v[2:3], 0, s[4:5]
	global_load_dwordx4 v[184:187], v[2:3], off
	v_lshl_add_u64 v[2:3], v[2:3], 0, s[4:5]
	global_load_dwordx4 v[188:191], v[2:3], off
	v_lshl_add_u64 v[2:3], v[2:3], 0, s[4:5]
	global_load_dwordx4 v[192:195], v[2:3], off
	v_lshl_add_u64 v[2:3], v[2:3], 0, s[4:5]
	global_load_dwordx4 v[196:199], v[2:3], off
	v_lshl_add_u64 v[2:3], v[2:3], 0, s[4:5]
	global_load_dwordx4 v[200:203], v[2:3], off
	v_lshl_add_u64 v[2:3], v[2:3], 0, s[4:5]
	v_cmp_gt_u32_e32 vcc, 32, v0
	s_and_saveexec_b64 s[8:9], vcc
	global_load_dwordx4 v[204:207], v[2:3], off
	s_mov_b64 exec, s[8:9]
	v_lshlrev_b32_e32 v2, 2, v0
	v_mov_b32_e32 v3, 0
	v_lshl_add_u64 v[2:3], s[62:63], 0, v[2:3]
	s_mov_b64 s[10:11], 0x1000
	v_lshl_add_u64 v[2:3], v[2:3], 0, s[10:11]
	global_load_dword v5, v[2:3], off
	global_load_dword v6, v[2:3], off offset:2048
	v_add_u32_e32 v7, 0x10000, v4
	v_add_u32_e32 v8, 0x10200, v147
	s_waitcnt vmcnt(0)
	ds_write_b128 v4, v[172:175] offset:0
	ds_write_b128 v4, v[176:179] offset:8192
	ds_write_b128 v4, v[180:183] offset:16384
	ds_write_b128 v4, v[184:187] offset:24576
	ds_write_b128 v4, v[188:191] offset:32768
	ds_write_b128 v4, v[192:195] offset:40960
	ds_write_b128 v4, v[196:199] offset:49152
	ds_write_b128 v4, v[200:203] offset:57344
	s_and_saveexec_b64 s[8:9], vcc
	ds_write_b128 v7, v[204:207]
	s_mov_b64 exec, s[8:9]
	ds_write_b32 v8, v5
	ds_write_b32 v8, v6 offset:2048
	s_cmpk_gt_i32 s92, 0xff
	s_cbranch_scc1 .LBB0_2639
	v_and_b32_e32 v1, 15, v0
	v_readlane_b32 s7, v235, 8
	s_add_i32 s0, 0, 0x13200
	v_readlane_b32 s5, v235, 52
	s_bfe_u32 s6, s7, 0x10006
	v_lshl_add_u32 v6, v1, 2, s0
	v_lshl_add_u32 v7, v146, 2, s0
	s_lshl_b32 s0, s5, 3
	s_and_b32 s9, s0, 0x1ffffff0
	s_lshl_b32 s4, s6, 9
	s_lshl_b32 s0, s6, 10
	v_readlane_b32 s16, v235, 9
	v_readlane_b32 s17, v235, 10
	s_add_u32 s0, s16, s0
	v_and_b32_e32 v54, 48, v0
	v_mov_b32_e32 v55, 0
	s_addc_u32 s1, s17, 0
	v_lshlrev_b32_e32 v2, 1, v54
	v_mov_b32_e32 v3, v55
	v_lshl_add_u64 v[2:3], s[0:1], 0, v[2:3]
	s_mov_b64 s[0:1], 0x22600000
	v_lshl_add_u64 v[56:57], v[2:3], 0, s[0:1]
	v_mul_u32_u24_e32 v2, 0x408, v1
	v_lshlrev_b32_e32 v9, 1, v2
	v_mbcnt_lo_u32_b32 v2, -1, 0
	v_mbcnt_hi_u32_b32 v10, -1, v2
	v_and_b32_e32 v4, 64, v10
	v_xor_b32_e32 v2, 16, v10
	v_add_u32_e32 v11, 64, v4
	v_cmp_lt_i32_e32 vcc, v2, v11
	s_lshl_b32 s0, s5, 10
	s_xor_b32 s5, s5, 1
	v_cndmask_b32_e32 v2, v10, v2, vcc
	s_add_i32 s8, 0, 0x11200
	s_and_b32 s12, s7, 0xffffffc0
	s_lshl_b32 s7, s5, 10
	v_lshlrev_b32_e32 v64, 2, v2
	v_xor_b32_e32 v2, 32, v10
	s_add_i32 s11, s8, s0
	s_add_i32 s8, s8, s7
	s_lshl_b32 s13, s5, 6
	v_or_b32_e32 v8, s4, v54
	v_cmp_lt_i32_e32 vcc, v2, v11
	s_add_u32 s4, s16, s4
	s_addc_u32 s5, s17, 0
	v_cndmask_b32_e32 v2, v10, v2, vcc
	v_lshlrev_b32_e32 v65, 2, v2
	v_lshl_add_u64 v[2:3], s[4:5], 0, v[54:55]
	s_mov_b64 s[4:5], 0x2a600000
	v_lshl_add_u64 v[58:59], v[2:3], 0, s[4:5]
	v_lshrrev_b32_e32 v2, 2, v0
	v_and_b32_e32 v2, 12, v2
	v_or_b32_e32 v3, v4, v2
	v_lshlrev_b32_e32 v69, 2, v3
	v_xor_b32_e32 v3, 1, v10
	v_cmp_lt_i32_e32 vcc, v3, v11
	s_lshl_b32 s4, s6, 11
	s_add_i32 s4, s4, 0
	v_cndmask_b32_e32 v3, v10, v3, vcc
	v_lshlrev_b32_e32 v70, 2, v3
	v_xor_b32_e32 v3, 2, v10
	v_cmp_lt_i32_e32 vcc, v3, v11
	s_add_i32 s4, s4, 0x10200
	v_lshl_add_u32 v67, v54, 2, s4
	v_cndmask_b32_e32 v3, v10, v3, vcc
	v_lshlrev_b32_e32 v71, 2, v3
	v_xor_b32_e32 v3, 4, v10
	v_cmp_lt_i32_e32 vcc, v3, v11
	v_lshlrev_b32_e32 v54, 13, v1
	s_cmp_eq_u32 s6, 0
	v_cndmask_b32_e32 v3, v10, v3, vcc
	v_lshlrev_b32_e32 v72, 2, v3
	v_xor_b32_e32 v3, 8, v10
	v_lshl_add_u64 v[4:5], s[16:17], 0, v[54:55]
	s_mov_b64 s[6:7], 0x2c600000
	v_cmp_lt_i32_e32 vcc, v3, v11
	v_lshlrev_b32_e32 v66, 4, v146
	s_cselect_b64 s[4:5], -1, 0
	v_lshl_add_u64 v[60:61], v[4:5], 0, s[6:7]
	v_lshlrev_b32_e32 v4, 1, v8
	v_cndmask_b32_e32 v3, v10, v3, vcc
	s_lshl_b32 s6, s92, 6
	v_cmp_gt_u32_e64 s[0:1], 16, v146
	v_add3_u32 v68, 0, v9, v4
	v_lshlrev_b32_e32 v73, 2, v3
	v_or_b32_e32 v74, 4, v69
	v_or_b32_e32 v75, 8, v69
	v_or_b32_e32 v76, 12, v69
	s_add_i32 s9, s6, s9
	s_lshl_b32 s10, s50, 6
	v_add_u32_e32 v77, s11, v66
	v_add_u32_e32 v78, s12, v7
	v_add_u32_e32 v79, s13, v6
	v_mov_b32_e32 v80, 0x358637bd
	s_mov_b32 s11, 0x800000
	s_mov_b32 s12, 0xc3e00000
	s_mov_b32 s13, 0x3fb8aa3b
	s_mov_b32 s14, 0xc2ce8ed0
	s_mov_b32 s15, 0x42b17218
	v_lshlrev_b32_e32 v54, 2, v2
	v_mov_b32_e32 v81, 0x43e00000
	v_mov_b32_e32 v82, 0x7f800000
	s_mov_b32 s16, s92
	v_readlane_b32 s18, v235, 11
	v_readlane_b32 s19, v235, 12
	s_branch .LBB0_2635

; DI void phase_topk(const Args& A, LAS unsigned char* lds, int bid, int G, int tid, int wave, int lane) {
;     ...
;         for (int r = wave; r < CAP; r += NWAVES) { const int s = list[r];
;             if ((s >> 10) == half) { const uint4* src = (const uint4*)(hb + (size_t)(b * SEQ + s) * DM) + lane; uint4* dstp = (uint4*)(xg + (size_t)(slot0 + r) * DM) + lane; dstp[0] = src[0]; } }
.LBB0_2747:
	s_add_i32 s26, s70, s21
	s_mov_b32 s25, 0
	v_mov_b32_e32 v2, s20
	ds_read_b32 v34, v2 offset:0
	ds_read_b32 v35, v2 offset:32
	ds_read_b32 v36, v2 offset:64
	ds_read_b32 v37, v2 offset:96
	ds_read_b32 v38, v2 offset:128
	ds_read_b32 v39, v2 offset:160
	ds_read_b32 v40, v2 offset:192
	ds_read_b32 v41, v2 offset:224
	ds_read_b32 v42, v2 offset:256
	ds_read_b32 v43, v2 offset:288
	ds_read_b32 v44, v2 offset:320
	ds_read_b32 v45, v2 offset:352
	ds_read_b32 v46, v2 offset:384
	ds_read_b32 v47, v2 offset:416
	ds_read_b32 v8, v2 offset:448
	ds_read_b32 v9, v2 offset:480
	s_waitcnt lgkmcnt(0)
	v_add_u32_e32 v4, s71, v34
	v_ashrrev_i32_e32 v5, 31, v4
	v_lshlrev_b64 v[4:5], 10, v[4:5]
	v_lshl_add_u64 v[4:5], v[14:15], 0, v[4:5]
	global_load_dwordx4 v[172:175], v[4:5], off
	v_add_u32_e32 v4, s71, v35
	v_ashrrev_i32_e32 v5, 31, v4
	v_lshlrev_b64 v[4:5], 10, v[4:5]
	v_lshl_add_u64 v[4:5], v[14:15], 0, v[4:5]
	global_load_dwordx4 v[176:179], v[4:5], off
	v_add_u32_e32 v4, s71, v36
	v_ashrrev_i32_e32 v5, 31, v4
	v_lshlrev_b64 v[4:5], 10, v[4:5]
	v_lshl_add_u64 v[4:5], v[14:15], 0, v[4:5]
	global_load_dwordx4 v[180:183], v[4:5], off
	v_add_u32_e32 v4, s71, v37
	v_ashrrev_i32_e32 v5, 31, v4
	v_lshlrev_b64 v[4:5], 10, v[4:5]
	v_lshl_add_u64 v[4:5], v[14:15], 0, v[4:5]
	global_load_dwordx4 v[184:187], v[4:5], off
	v_add_u32_e32 v4, s71, v38
	v_ashrrev_i32_e32 v5, 31, v4
	v_lshlrev_b64 v[4:5], 10, v[4:5]
	v_lshl_add_u64 v[4:5], v[14:15], 0, v[4:5]
	global_load_dwordx4 v[188:191], v[4:5], off
	v_add_u32_e32 v4, s71, v39
	v_ashrrev_i32_e32 v5, 31, v4
	v_lshlrev_b64 v[4:5], 10, v[4:5]
	v_lshl_add_u64 v[4:5], v[14:15], 0, v[4:5]
	global_load_dwordx4 v[192:195], v[4:5], off
	v_add_u32_e32 v4, s71, v40
	v_ashrrev_i32_e32 v5, 31, v4
	v_lshlrev_b64 v[4:5], 10, v[4:5]
	v_lshl_add_u64 v[4:5], v[14:15], 0, v[4:5]
	global_load_dwordx4 v[196:199], v[4:5], off
	v_add_u32_e32 v4, s71, v41
	v_ashrrev_i32_e32 v5, 31, v4
	v_lshlrev_b64 v[4:5], 10, v[4:5]
	v_lshl_add_u64 v[4:5], v[14:15], 0, v[4:5]
	global_load_dwordx4 v[200:203], v[4:5], off
	v_add_u32_e32 v4, s71, v42
	v_ashrrev_i32_e32 v5, 31, v4
	v_lshlrev_b64 v[4:5], 10, v[4:5]
	v_lshl_add_u64 v[4:5], v[14:15], 0, v[4:5]
	global_load_dwordx4 v[204:207], v[4:5], off
	v_add_u32_e32 v4, s71, v43
	v_ashrrev_i32_e32 v5, 31, v4
	v_lshlrev_b64 v[4:5], 10, v[4:5]
	v_lshl_add_u64 v[4:5], v[14:15], 0, v[4:5]
	global_load_dwordx4 v[208:211], v[4:5], off
	v_add_u32_e32 v4, s71, v44
	v_ashrrev_i32_e32 v5, 31, v4
	v_lshlrev_b64 v[4:5], 10, v[4:5]
	v_lshl_add_u64 v[4:5], v[14:15], 0, v[4:5]
	global_load_dwordx4 v[212:215], v[4:5], off
	v_add_u32_e32 v4, s71, v45
	v_ashrrev_i32_e32 v5, 31, v4
	v_lshlrev_b64 v[4:5], 10, v[4:5]
	v_lshl_add_u64 v[4:5], v[14:15], 0, v[4:5]
	global_load_dwordx4 v[216:219], v[4:5], off
	v_add_u32_e32 v4, s71, v46
	v_ashrrev_i32_e32 v5, 31, v4
	v_lshlrev_b64 v[4:5], 10, v[4:5]
	v_lshl_add_u64 v[4:5], v[14:15], 0, v[4:5]
	global_load_dwordx4 v[220:223], v[4:5], off
	v_add_u32_e32 v4, s71, v47
	v_ashrrev_i32_e32 v5, 31, v4
	v_lshlrev_b64 v[4:5], 10, v[4:5]
	v_lshl_add_u64 v[4:5], v[14:15], 0, v[4:5]
	global_load_dwordx4 v[224:227], v[4:5], off
	v_add_u32_e32 v4, s71, v8
	v_ashrrev_i32_e32 v5, 31, v4
	v_lshlrev_b64 v[4:5], 10, v[4:5]
	v_lshl_add_u64 v[4:5], v[14:15], 0, v[4:5]
	global_load_dwordx4 v[228:231], v[4:5], off
	v_add_u32_e32 v4, s71, v9
	v_ashrrev_i32_e32 v5, 31, v4
	v_lshlrev_b64 v[4:5], 10, v[4:5]
	v_lshl_add_u64 v[4:5], v[14:15], 0, v[4:5]
	global_load_dwordx4 v[236:239], v[4:5], off
	s_waitcnt vmcnt(0)
	v_readfirstlane_b32 s27, v34
	s_add_i32 s24, s26, 0
	s_lshl_b32 s24, s24, 10
	s_ashr_i32 s27, s27, 10
	s_cmp_lg_u32 s27, s69
	s_cbranch_scc1 .Lgs1_0
	v_lshl_add_u64 v[6:7], v[16:17], 0, s[24:25]
	global_store_dwordx4 v[6:7], v[172:175], off
.Lgs1_0:
	v_readfirstlane_b32 s27, v35
	s_add_i32 s24, s26, 8
	s_lshl_b32 s24, s24, 10
	s_ashr_i32 s27, s27, 10
	s_cmp_lg_u32 s27, s69
	s_cbranch_scc1 .Lgs1_1
	v_lshl_add_u64 v[6:7], v[16:17], 0, s[24:25]
	global_store_dwordx4 v[6:7], v[176:179], off
.Lgs1_1:
	v_readfirstlane_b32 s27, v36
	s_add_i32 s24, s26, 16
	s_lshl_b32 s24, s24, 10
	s_ashr_i32 s27, s27, 10
	s_cmp_lg_u32 s27, s69
	s_cbranch_scc1 .Lgs1_2
	v_lshl_add_u64 v[6:7], v[16:17], 0, s[24:25]
	global_store_dwordx4 v[6:7], v[180:183], off
.Lgs1_2:
	v_readfirstlane_b32 s27, v37
	s_add_i32 s24, s26, 24
	s_lshl_b32 s24, s24, 10
	s_ashr_i32 s27, s27, 10
	s_cmp_lg_u32 s27, s69
	s_cbranch_scc1 .Lgs1_3
	v_lshl_add_u64 v[6:7], v[16:17], 0, s[24:25]
	global_store_dwordx4 v[6:7], v[184:187], off
.Lgs1_3:
	v_readfirstlane_b32 s27, v38
	s_add_i32 s24, s26, 32
	s_lshl_b32 s24, s24, 10
	s_ashr_i32 s27, s27, 10
	s_cmp_lg_u32 s27, s69
	s_cbranch_scc1 .Lgs1_4
	v_lshl_add_u64 v[6:7], v[16:17], 0, s[24:25]
	global_store_dwordx4 v[6:7], v[188:191], off
.Lgs1_4:
	v_readfirstlane_b32 s27, v39
	s_add_i32 s24, s26, 40
	s_lshl_b32 s24, s24, 10
	s_ashr_i32 s27, s27, 10
	s_cmp_lg_u32 s27, s69
	s_cbranch_scc1 .Lgs1_5
	v_lshl_add_u64 v[6:7], v[16:17], 0, s[24:25]
	global_store_dwordx4 v[6:7], v[192:195], off
.Lgs1_5:
	v_readfirstlane_b32 s27, v40
	s_add_i32 s24, s26, 48
	s_lshl_b32 s24, s24, 10
	s_ashr_i32 s27, s27, 10
	s_cmp_lg_u32 s27, s69
	s_cbranch_scc1 .Lgs1_6
	v_lshl_add_u64 v[6:7], v[16:17], 0, s[24:25]
	global_store_dwordx4 v[6:7], v[196:199], off
.Lgs1_6:
	v_readfirstlane_b32 s27, v41
	s_add_i32 s24, s26, 56
	s_lshl_b32 s24, s24, 10
	s_ashr_i32 s27, s27, 10
	s_cmp_lg_u32 s27, s69
	s_cbranch_scc1 .Lgs1_7
	v_lshl_add_u64 v[6:7], v[16:17], 0, s[24:25]
	global_store_dwordx4 v[6:7], v[200:203], off
; DI void phase_topk(const Args& A, LAS unsigned char* lds, int bid, int G, int tid, int wave, int lane) {
;     ...
;         for (int r = wave; r < CAP; r += NWAVES) { const int s = list[r];
;             if ((s >> 10) == half) { const uint4* src = (const uint4*)(hb + (size_t)(b * SEQ + s) * DM) + lane; uint4* dstp = (uint4*)(xg + (size_t)(slot0 + r) * DM) + lane; dstp[0] = src[0]; } }
.Lgs1_7:
	v_readfirstlane_b32 s27, v42
	s_add_i32 s24, s26, 64
	s_lshl_b32 s24, s24, 10
	s_ashr_i32 s27, s27, 10
	s_cmp_lg_u32 s27, s69
	s_cbranch_scc1 .Lgs1_8
	v_lshl_add_u64 v[6:7], v[16:17], 0, s[24:25]
	global_store_dwordx4 v[6:7], v[204:207], off
.Lgs1_8:
	v_readfirstlane_b32 s27, v43
	s_add_i32 s24, s26, 72
	s_lshl_b32 s24, s24, 10
	s_ashr_i32 s27, s27, 10
	s_cmp_lg_u32 s27, s69
	s_cbranch_scc1 .Lgs1_9
	v_lshl_add_u64 v[6:7], v[16:17], 0, s[24:25]
	global_store_dwordx4 v[6:7], v[208:211], off
.Lgs1_9:
	v_readfirstlane_b32 s27, v44
	s_add_i32 s24, s26, 80
	s_lshl_b32 s24, s24, 10
	s_ashr_i32 s27, s27, 10
	s_cmp_lg_u32 s27, s69
	s_cbranch_scc1 .Lgs1_10
	v_lshl_add_u64 v[6:7], v[16:17], 0, s[24:25]
	global_store_dwordx4 v[6:7], v[212:215], off
.Lgs1_10:
	v_readfirstlane_b32 s27, v45
	s_add_i32 s24, s26, 88
	s_lshl_b32 s24, s24, 10
	s_ashr_i32 s27, s27, 10
	s_cmp_lg_u32 s27, s69
	s_cbranch_scc1 .Lgs1_11
	v_lshl_add_u64 v[6:7], v[16:17], 0, s[24:25]
	global_store_dwordx4 v[6:7], v[216:219], off
.Lgs1_11:
	v_readfirstlane_b32 s27, v46
	s_add_i32 s24, s26, 96
	s_lshl_b32 s24, s24, 10
	s_ashr_i32 s27, s27, 10
	s_cmp_lg_u32 s27, s69
	s_cbranch_scc1 .Lgs1_12
	v_lshl_add_u64 v[6:7], v[16:17], 0, s[24:25]
	global_store_dwordx4 v[6:7], v[220:223], off
.Lgs1_12:
	v_readfirstlane_b32 s27, v47
	s_add_i32 s24, s26, 104
	s_lshl_b32 s24, s24, 10
	s_ashr_i32 s27, s27, 10
	s_cmp_lg_u32 s27, s69
	s_cbranch_scc1 .Lgs1_13
	v_lshl_add_u64 v[6:7], v[16:17], 0, s[24:25]
	global_store_dwordx4 v[6:7], v[224:227], off
.Lgs1_13:
	v_readfirstlane_b32 s27, v8
	s_add_i32 s24, s26, 112
	s_lshl_b32 s24, s24, 10
	s_ashr_i32 s27, s27, 10
	s_cmp_lg_u32 s27, s69
	s_cbranch_scc1 .Lgs1_14
	v_lshl_add_u64 v[6:7], v[16:17], 0, s[24:25]
	global_store_dwordx4 v[6:7], v[228:231], off
.Lgs1_14:
	v_readfirstlane_b32 s27, v9
	s_add_i32 s24, s26, 120
	s_lshl_b32 s24, s24, 10
	s_ashr_i32 s27, s27, 10
	s_cmp_lg_u32 s27, s69
	s_cbranch_scc1 .Lgs1_15
	v_lshl_add_u64 v[6:7], v[16:17], 0, s[24:25]
	global_store_dwordx4 v[6:7], v[236:239], off
.Lgs1_15:
	ds_read_b32 v34, v2 offset:512
	ds_read_b32 v35, v2 offset:544
	ds_read_b32 v36, v2 offset:576
	ds_read_b32 v37, v2 offset:608
	ds_read_b32 v38, v2 offset:640
	ds_read_b32 v39, v2 offset:672
	ds_read_b32 v40, v2 offset:704
	ds_read_b32 v41, v2 offset:736
	ds_read_b32 v42, v2 offset:768
	ds_read_b32 v43, v2 offset:800
	ds_read_b32 v44, v2 offset:832
	ds_read_b32 v45, v2 offset:864
	ds_read_b32 v46, v2 offset:896
	ds_read_b32 v47, v2 offset:928
	ds_read_b32 v8, v2 offset:960
	ds_read_b32 v9, v2 offset:992
	s_waitcnt lgkmcnt(0)
	v_add_u32_e32 v4, s71, v34
	v_ashrrev_i32_e32 v5, 31, v4
	v_lshlrev_b64 v[4:5], 10, v[4:5]
	v_lshl_add_u64 v[4:5], v[14:15], 0, v[4:5]
	global_load_dwordx4 v[172:175], v[4:5], off
	v_add_u32_e32 v4, s71, v35
	v_ashrrev_i32_e32 v5, 31, v4
	v_lshlrev_b64 v[4:5], 10, v[4:5]
	v_lshl_add_u64 v[4:5], v[14:15], 0, v[4:5]
	global_load_dwordx4 v[176:179], v[4:5], off
	v_add_u32_e32 v4, s71, v36
	v_ashrrev_i32_e32 v5, 31, v4
	v_lshlrev_b64 v[4:5], 10, v[4:5]
	v_lshl_add_u64 v[4:5], v[14:15], 0, v[4:5]
	global_load_dwordx4 v[180:183], v[4:5], off
	v_add_u32_e32 v4, s71, v37
	v_ashrrev_i32_e32 v5, 31, v4
	v_lshlrev_b64 v[4:5], 10, v[4:5]
	v_lshl_add_u64 v[4:5], v[14:15], 0, v[4:5]
	global_load_dwordx4 v[184:187], v[4:5], off
	v_add_u32_e32 v4, s71, v38
	v_ashrrev_i32_e32 v5, 31, v4
	v_lshlrev_b64 v[4:5], 10, v[4:5]
	v_lshl_add_u64 v[4:5], v[14:15], 0, v[4:5]
	global_load_dwordx4 v[188:191], v[4:5], off
	v_add_u32_e32 v4, s71, v39
	v_ashrrev_i32_e32 v5, 31, v4
	v_lshlrev_b64 v[4:5], 10, v[4:5]
	v_lshl_add_u64 v[4:5], v[14:15], 0, v[4:5]
	global_load_dwordx4 v[192:195], v[4:5], off
	v_add_u32_e32 v4, s71, v40
	v_ashrrev_i32_e32 v5, 31, v4
	v_lshlrev_b64 v[4:5], 10, v[4:5]
	v_lshl_add_u64 v[4:5], v[14:15], 0, v[4:5]
	global_load_dwordx4 v[196:199], v[4:5], off
	v_add_u32_e32 v4, s71, v41
	v_ashrrev_i32_e32 v5, 31, v4
	v_lshlrev_b64 v[4:5], 10, v[4:5]
	v_lshl_add_u64 v[4:5], v[14:15], 0, v[4:5]
	global_load_dwordx4 v[200:203], v[4:5], off
	v_add_u32_e32 v4, s71, v42
	v_ashrrev_i32_e32 v5, 31, v4
	v_lshlrev_b64 v[4:5], 10, v[4:5]
	v_lshl_add_u64 v[4:5], v[14:15], 0, v[4:5]
	global_load_dwordx4 v[204:207], v[4:5], off
	v_add_u32_e32 v4, s71, v43
	v_ashrrev_i32_e32 v5, 31, v4
	v_lshlrev_b64 v[4:5], 10, v[4:5]
	v_lshl_add_u64 v[4:5], v[14:15], 0, v[4:5]
	global_load_dwordx4 v[208:211], v[4:5], off
	v_add_u32_e32 v4, s71, v44
	v_ashrrev_i32_e32 v5, 31, v4
	v_lshlrev_b64 v[4:5], 10, v[4:5]
	v_lshl_add_u64 v[4:5], v[14:15], 0, v[4:5]
	global_load_dwordx4 v[212:215], v[4:5], off
	v_add_u32_e32 v4, s71, v45
	v_ashrrev_i32_e32 v5, 31, v4
	v_lshlrev_b64 v[4:5], 10, v[4:5]
	v_lshl_add_u64 v[4:5], v[14:15], 0, v[4:5]
	global_load_dwordx4 v[216:219], v[4:5], off
	v_add_u32_e32 v4, s71, v46
	v_ashrrev_i32_e32 v5, 31, v4
	v_lshlrev_b64 v[4:5], 10, v[4:5]
	v_lshl_add_u64 v[4:5], v[14:15], 0, v[4:5]
	global_load_dwordx4 v[220:223], v[4:5], off
	v_add_u32_e32 v4, s71, v47
	v_ashrrev_i32_e32 v5, 31, v4
	v_lshlrev_b64 v[4:5], 10, v[4:5]
	v_lshl_add_u64 v[4:5], v[14:15], 0, v[4:5]
	global_load_dwordx4 v[224:227], v[4:5], off
	v_add_u32_e32 v4, s71, v8
	v_ashrrev_i32_e32 v5, 31, v4
	v_lshlrev_b64 v[4:5], 10, v[4:5]
	v_lshl_add_u64 v[4:5], v[14:15], 0, v[4:5]
	global_load_dwordx4 v[228:231], v[4:5], off
	v_add_u32_e32 v4, s71, v9
	v_ashrrev_i32_e32 v5, 31, v4
	v_lshlrev_b64 v[4:5], 10, v[4:5]
	v_lshl_add_u64 v[4:5], v[14:15], 0, v[4:5]
	global_load_dwordx4 v[236:239], v[4:5], off
	s_waitcnt vmcnt(0)
	v_readfirstlane_b32 s27, v34
	s_add_i32 s24, s26, 128
	s_lshl_b32 s24, s24, 10
	s_ashr_i32 s27, s27, 10
	s_cmp_lg_u32 s27, s69
	s_cbranch_scc1 .Lgs1_16
	v_lshl_add_u64 v[6:7], v[16:17], 0, s[24:25]
	global_store_dwordx4 v[6:7], v[172:175], off
; DI void phase_topk(const Args& A, LAS unsigned char* lds, int bid, int G, int tid, int wave, int lane) {
;     ...
;         for (int r = wave; r < CAP; r += NWAVES) { const int s = list[r];
;             if ((s >> 10) == half) { const uint4* src = (const uint4*)(hb + (size_t)(b * SEQ + s) * DM) + lane; uint4* dstp = (uint4*)(xg + (size_t)(slot0 + r) * DM) + lane; dstp[0] = src[0]; } }
.Lgs1_16:
	v_readfirstlane_b32 s27, v35
	s_add_i32 s24, s26, 136
	s_lshl_b32 s24, s24, 10
	s_ashr_i32 s27, s27, 10
	s_cmp_lg_u32 s27, s69
	s_cbranch_scc1 .Lgs1_17
	v_lshl_add_u64 v[6:7], v[16:17], 0, s[24:25]
	global_store_dwordx4 v[6:7], v[176:179], off
.Lgs1_17:
	v_readfirstlane_b32 s27, v36
	s_add_i32 s24, s26, 144
	s_lshl_b32 s24, s24, 10
	s_ashr_i32 s27, s27, 10
	s_cmp_lg_u32 s27, s69
	s_cbranch_scc1 .Lgs1_18
	v_lshl_add_u64 v[6:7], v[16:17], 0, s[24:25]
	global_store_dwordx4 v[6:7], v[180:183], off
.Lgs1_18:
	v_readfirstlane_b32 s27, v37
	s_add_i32 s24, s26, 152
	s_lshl_b32 s24, s24, 10
	s_ashr_i32 s27, s27, 10
	s_cmp_lg_u32 s27, s69
	s_cbranch_scc1 .Lgs1_19
	v_lshl_add_u64 v[6:7], v[16:17], 0, s[24:25]
	global_store_dwordx4 v[6:7], v[184:187], off
.Lgs1_19:
	v_readfirstlane_b32 s27, v38
	s_add_i32 s24, s26, 160
	s_lshl_b32 s24, s24, 10
	s_ashr_i32 s27, s27, 10
	s_cmp_lg_u32 s27, s69
	s_cbranch_scc1 .Lgs1_20
	v_lshl_add_u64 v[6:7], v[16:17], 0, s[24:25]
	global_store_dwordx4 v[6:7], v[188:191], off
.Lgs1_20:
	v_readfirstlane_b32 s27, v39
	s_add_i32 s24, s26, 168
	s_lshl_b32 s24, s24, 10
	s_ashr_i32 s27, s27, 10
	s_cmp_lg_u32 s27, s69
	s_cbranch_scc1 .Lgs1_21
	v_lshl_add_u64 v[6:7], v[16:17], 0, s[24:25]
	global_store_dwordx4 v[6:7], v[192:195], off
.Lgs1_21:
	v_readfirstlane_b32 s27, v40
	s_add_i32 s24, s26, 176
	s_lshl_b32 s24, s24, 10
	s_ashr_i32 s27, s27, 10
	s_cmp_lg_u32 s27, s69
	s_cbranch_scc1 .Lgs1_22
	v_lshl_add_u64 v[6:7], v[16:17], 0, s[24:25]
	global_store_dwordx4 v[6:7], v[196:199], off
.Lgs1_22:
	v_readfirstlane_b32 s27, v41
	s_add_i32 s24, s26, 184
	s_lshl_b32 s24, s24, 10
	s_ashr_i32 s27, s27, 10
	s_cmp_lg_u32 s27, s69
	s_cbranch_scc1 .Lgs1_23
	v_lshl_add_u64 v[6:7], v[16:17], 0, s[24:25]
	global_store_dwordx4 v[6:7], v[200:203], off
.Lgs1_23:
	v_readfirstlane_b32 s27, v42
	s_add_i32 s24, s26, 192
	s_lshl_b32 s24, s24, 10
	s_ashr_i32 s27, s27, 10
	s_cmp_lg_u32 s27, s69
	s_cbranch_scc1 .Lgs1_24
	v_lshl_add_u64 v[6:7], v[16:17], 0, s[24:25]
	global_store_dwordx4 v[6:7], v[204:207], off
.Lgs1_24:
	v_readfirstlane_b32 s27, v43
	s_add_i32 s24, s26, 200
	s_lshl_b32 s24, s24, 10
	s_ashr_i32 s27, s27, 10
	s_cmp_lg_u32 s27, s69
	s_cbranch_scc1 .Lgs1_25
	v_lshl_add_u64 v[6:7], v[16:17], 0, s[24:25]
	global_store_dwordx4 v[6:7], v[208:211], off
.Lgs1_25:
	v_readfirstlane_b32 s27, v44
	s_add_i32 s24, s26, 208
	s_lshl_b32 s24, s24, 10
	s_ashr_i32 s27, s27, 10
	s_cmp_lg_u32 s27, s69
	s_cbranch_scc1 .Lgs1_26
	v_lshl_add_u64 v[6:7], v[16:17], 0, s[24:25]
	global_store_dwordx4 v[6:7], v[212:215], off
.Lgs1_26:
	v_readfirstlane_b32 s27, v45
	s_add_i32 s24, s26, 216
	s_lshl_b32 s24, s24, 10
	s_ashr_i32 s27, s27, 10
	s_cmp_lg_u32 s27, s69
	s_cbranch_scc1 .Lgs1_27
	v_lshl_add_u64 v[6:7], v[16:17], 0, s[24:25]
	global_store_dwordx4 v[6:7], v[216:219], off
.Lgs1_27:
	v_readfirstlane_b32 s27, v46
	s_add_i32 s24, s26, 224
	s_lshl_b32 s24, s24, 10
	s_ashr_i32 s27, s27, 10
	s_cmp_lg_u32 s27, s69
	s_cbranch_scc1 .Lgs1_28
	v_lshl_add_u64 v[6:7], v[16:17], 0, s[24:25]
	global_store_dwordx4 v[6:7], v[220:223], off
.Lgs1_28:
	v_readfirstlane_b32 s27, v47
	s_add_i32 s24, s26, 232
	s_lshl_b32 s24, s24, 10
	s_ashr_i32 s27, s27, 10
	s_cmp_lg_u32 s27, s69
	s_cbranch_scc1 .Lgs1_29
	v_lshl_add_u64 v[6:7], v[16:17], 0, s[24:25]
	global_store_dwordx4 v[6:7], v[224:227], off
.Lgs1_29:
	v_readfirstlane_b32 s27, v8
	s_add_i32 s24, s26, 240
	s_lshl_b32 s24, s24, 10
	s_ashr_i32 s27, s27, 10
	s_cmp_lg_u32 s27, s69
	s_cbranch_scc1 .Lgs1_30
	v_lshl_add_u64 v[6:7], v[16:17], 0, s[24:25]
	global_store_dwordx4 v[6:7], v[228:231], off
.Lgs1_30:
	v_readfirstlane_b32 s27, v9
	s_add_i32 s24, s26, 248
	s_lshl_b32 s24, s24, 10
	s_ashr_i32 s27, s27, 10
	s_cmp_lg_u32 s27, s69
	s_cbranch_scc1 .Lgs1_31
	v_lshl_add_u64 v[6:7], v[16:17], 0, s[24:25]
	global_store_dwordx4 v[6:7], v[236:239], off
